# 4 edge slots per row per step instead of 6 (fewer idle slot checks per sweep step)
# speedup vs baseline: 1.1150x; 1.0038x over previous
.Lhq0_phase:
	s_mov_b32 s26, 0x8000
	s_cmp_eq_u32 s27, 3
	s_cselect_b32 s26, 21846, s26
	s_cmp_eq_u32 s27, 4
	s_cselect_b32 s26, 16384, s26
	v_sub_u32_e32 v2, v51, v46
	v_lshrrev_b32_e32 v2, 3, v2
	v_mul_u32_u24_e32 v2, s26, v2
	v_lshrrev_b32_e32 v2, 16, v2
	v_lshl_add_u32 v5, v2, 3, v46
.Lhq0_s0_top:
	v_sub_u32_e32 v2, v5, v46
	ds_read_b64 v[6:7], v46
	ds_read_b64 v[8:9], v46 offset:8
	ds_read_b64 v[10:11], v46 offset:16
	ds_read_b64 v[12:13], v46 offset:24
	v_cmp_lt_i32_e64 s[30:31], 0, v2
	s_and_b64 s[30:31], s[30:31], exec
	s_cbranch_scc0 .Lhq0_s0_done
	v_cmp_lt_i32_e64 s[32:33], 8, v2
	v_cmp_lt_i32_e64 s[34:35], 16, v2
	v_cmp_lt_i32_e64 s[36:37], 24, v2
	v_cmp_lt_i32_e64 s[42:43], 32, v2
	v_add_u32_e32 v46, 32, v46
	v_min_i32_e32 v46, v46, v5
	s_waitcnt lgkmcnt(0)
	s_mov_b64 exec, s[30:31]
	v_lshlrev_b32_e32 v3, 7, v6
	v_and_or_b32 v3, v3, s29, v1
	global_load_dwordx4 v[18:21], v3, s[8:9]
	s_and_b64 exec, s[32:33], s[32:33]
	s_cbranch_scc0 .Lhq0_s0_ld_done
	v_lshlrev_b32_e32 v4, 7, v8
	v_and_or_b32 v4, v4, s29, v1
	global_load_dwordx4 v[22:25], v4, s[8:9]
	s_and_b64 exec, s[34:35], s[34:35]
	s_cbranch_scc0 .Lhq0_s0_ld_done
	v_lshlrev_b32_e32 v3, 7, v10
	v_and_or_b32 v3, v3, s29, v1
	global_load_dwordx4 v[26:29], v3, s[8:9]
	s_and_b64 exec, s[36:37], s[36:37]
	s_cbranch_scc0 .Lhq0_s0_ld_done
	v_lshlrev_b32_e32 v4, 7, v12
	v_and_or_b32 v4, v4, s29, v1
	global_load_dwordx4 v[30:33], v4, s[8:9]
.Lhq0_s0_ld_done:
	s_waitcnt vmcnt(0)
	s_mov_b64 exec, s[30:31]
	v_cvt_f32_f16_e32 v42, v18
	v_cvt_f32_f16_sdwa v43, v18 dst_sel:DWORD dst_unused:UNUSED_PAD src0_sel:WORD_1
	v_cvt_f32_f16_e32 v44, v20
	v_cvt_f32_f16_sdwa v45, v20 dst_sel:DWORD dst_unused:UNUSED_PAD src0_sel:WORD_1
	v_cvt_f32_f16_e32 v18, v19
	v_cvt_f32_f16_sdwa v19, v19 dst_sel:DWORD dst_unused:UNUSED_PAD src0_sel:WORD_1
	v_cvt_f32_f16_e32 v20, v21
	v_cvt_f32_f16_sdwa v21, v21 dst_sel:DWORD dst_unused:UNUSED_PAD src0_sel:WORD_1
	v_fma_f32 v56, v7, v42, v56
	v_fma_f32 v57, v7, v43, v57
	v_fma_f32 v58, v7, v18, v58
	v_fma_f32 v59, v7, v19, v59
	v_fma_f32 v60, v7, v44, v60
	v_fma_f32 v61, v7, v45, v61
	v_fma_f32 v62, v7, v20, v62
	v_fma_f32 v63, v7, v21, v63
	s_and_b64 exec, s[32:33], s[32:33]
	s_cbranch_scc0 .Lhq0_s0_cp_done
	v_cvt_f32_f16_e32 v42, v22
	v_cvt_f32_f16_sdwa v43, v22 dst_sel:DWORD dst_unused:UNUSED_PAD src0_sel:WORD_1
	v_cvt_f32_f16_e32 v44, v24
	v_cvt_f32_f16_sdwa v45, v24 dst_sel:DWORD dst_unused:UNUSED_PAD src0_sel:WORD_1
	v_cvt_f32_f16_e32 v22, v23
	v_cvt_f32_f16_sdwa v23, v23 dst_sel:DWORD dst_unused:UNUSED_PAD src0_sel:WORD_1
	v_cvt_f32_f16_e32 v24, v25
	v_cvt_f32_f16_sdwa v25, v25 dst_sel:DWORD dst_unused:UNUSED_PAD src0_sel:WORD_1
	v_fma_f32 v56, v9, v42, v56
	v_fma_f32 v57, v9, v43, v57
	v_fma_f32 v58, v9, v22, v58
	v_fma_f32 v59, v9, v23, v59
	v_fma_f32 v60, v9, v44, v60
	v_fma_f32 v61, v9, v45, v61
	v_fma_f32 v62, v9, v24, v62
	v_fma_f32 v63, v9, v25, v63
	s_and_b64 exec, s[34:35], s[34:35]
	s_cbranch_scc0 .Lhq0_s0_cp_done
	v_cvt_f32_f16_e32 v42, v26
	v_cvt_f32_f16_sdwa v43, v26 dst_sel:DWORD dst_unused:UNUSED_PAD src0_sel:WORD_1
	v_cvt_f32_f16_e32 v44, v28
	v_cvt_f32_f16_sdwa v45, v28 dst_sel:DWORD dst_unused:UNUSED_PAD src0_sel:WORD_1
	v_cvt_f32_f16_e32 v26, v27
	v_cvt_f32_f16_sdwa v27, v27 dst_sel:DWORD dst_unused:UNUSED_PAD src0_sel:WORD_1
	v_cvt_f32_f16_e32 v28, v29
	v_cvt_f32_f16_sdwa v29, v29 dst_sel:DWORD dst_unused:UNUSED_PAD src0_sel:WORD_1
	v_fma_f32 v56, v11, v42, v56
	v_fma_f32 v57, v11, v43, v57
	v_fma_f32 v58, v11, v26, v58
	v_fma_f32 v59, v11, v27, v59
	v_fma_f32 v60, v11, v44, v60
	v_fma_f32 v61, v11, v45, v61
	v_fma_f32 v62, v11, v28, v62
	v_fma_f32 v63, v11, v29, v63
	s_and_b64 exec, s[36:37], s[36:37]
	s_cbranch_scc0 .Lhq0_s0_cp_done
	v_cvt_f32_f16_e32 v42, v30
	v_cvt_f32_f16_sdwa v43, v30 dst_sel:DWORD dst_unused:UNUSED_PAD src0_sel:WORD_1
	v_cvt_f32_f16_e32 v44, v32
	v_cvt_f32_f16_sdwa v45, v32 dst_sel:DWORD dst_unused:UNUSED_PAD src0_sel:WORD_1
	v_cvt_f32_f16_e32 v30, v31
	v_cvt_f32_f16_sdwa v31, v31 dst_sel:DWORD dst_unused:UNUSED_PAD src0_sel:WORD_1
	v_cvt_f32_f16_e32 v32, v33
	v_cvt_f32_f16_sdwa v33, v33 dst_sel:DWORD dst_unused:UNUSED_PAD src0_sel:WORD_1
	v_fma_f32 v56, v13, v42, v56
	v_fma_f32 v57, v13, v43, v57
	v_fma_f32 v58, v13, v30, v58
	v_fma_f32 v59, v13, v31, v59
	v_fma_f32 v60, v13, v44, v60
	v_fma_f32 v61, v13, v45, v61
	v_fma_f32 v62, v13, v32, v62
	v_fma_f32 v63, v13, v33, v63
.Lhq0_s0_cp_done:
	s_and_b64 exec, s[42:43], s[42:43]
	s_cbranch_scc1 .Lhq0_s0_top

.Lhq0_s1_top:
	v_sub_u32_e32 v2, v5, v47
	ds_read_b64 v[6:7], v47
	ds_read_b64 v[8:9], v47 offset:8
	ds_read_b64 v[10:11], v47 offset:16
	ds_read_b64 v[12:13], v47 offset:24
	v_cmp_lt_i32_e64 s[30:31], 0, v2
	s_and_b64 s[30:31], s[30:31], exec
	s_cbranch_scc0 .Lhq0_s1_done
	v_cmp_lt_i32_e64 s[32:33], 8, v2
	v_cmp_lt_i32_e64 s[34:35], 16, v2
	v_cmp_lt_i32_e64 s[36:37], 24, v2
	v_cmp_lt_i32_e64 s[42:43], 32, v2
	v_add_u32_e32 v47, 32, v47
	v_min_i32_e32 v47, v47, v5
	s_waitcnt lgkmcnt(0)
	s_mov_b64 exec, s[30:31]
	v_lshlrev_b32_e32 v3, 7, v6
	v_and_or_b32 v3, v3, s29, v1
	global_load_dwordx4 v[18:21], v3, s[8:9]
	s_and_b64 exec, s[32:33], s[32:33]
	s_cbranch_scc0 .Lhq0_s1_ld_done
	v_lshlrev_b32_e32 v4, 7, v8
	v_and_or_b32 v4, v4, s29, v1
	global_load_dwordx4 v[22:25], v4, s[8:9]
	s_and_b64 exec, s[34:35], s[34:35]
	s_cbranch_scc0 .Lhq0_s1_ld_done
	v_lshlrev_b32_e32 v3, 7, v10
	v_and_or_b32 v3, v3, s29, v1
	global_load_dwordx4 v[26:29], v3, s[8:9]
	s_and_b64 exec, s[36:37], s[36:37]
	s_cbranch_scc0 .Lhq0_s1_ld_done
	v_lshlrev_b32_e32 v4, 7, v12
	v_and_or_b32 v4, v4, s29, v1
	global_load_dwordx4 v[30:33], v4, s[8:9]
.Lhq0_s1_ld_done:
	s_waitcnt vmcnt(0)
	s_mov_b64 exec, s[30:31]
	v_cvt_f32_f16_e32 v42, v18
	v_cvt_f32_f16_sdwa v43, v18 dst_sel:DWORD dst_unused:UNUSED_PAD src0_sel:WORD_1
	v_cvt_f32_f16_e32 v44, v20
	v_cvt_f32_f16_sdwa v45, v20 dst_sel:DWORD dst_unused:UNUSED_PAD src0_sel:WORD_1
	v_cvt_f32_f16_e32 v18, v19
	v_cvt_f32_f16_sdwa v19, v19 dst_sel:DWORD dst_unused:UNUSED_PAD src0_sel:WORD_1
	v_cvt_f32_f16_e32 v20, v21
	v_cvt_f32_f16_sdwa v21, v21 dst_sel:DWORD dst_unused:UNUSED_PAD src0_sel:WORD_1
	v_fma_f32 v64, v7, v42, v64
	v_fma_f32 v65, v7, v43, v65
	v_fma_f32 v66, v7, v18, v66
	v_fma_f32 v67, v7, v19, v67
	v_fma_f32 v68, v7, v44, v68
	v_fma_f32 v69, v7, v45, v69
	v_fma_f32 v70, v7, v20, v70
	v_fma_f32 v71, v7, v21, v71
	s_and_b64 exec, s[32:33], s[32:33]
	s_cbranch_scc0 .Lhq0_s1_cp_done
	v_cvt_f32_f16_e32 v42, v22
	v_cvt_f32_f16_sdwa v43, v22 dst_sel:DWORD dst_unused:UNUSED_PAD src0_sel:WORD_1
	v_cvt_f32_f16_e32 v44, v24
	v_cvt_f32_f16_sdwa v45, v24 dst_sel:DWORD dst_unused:UNUSED_PAD src0_sel:WORD_1
	v_cvt_f32_f16_e32 v22, v23
	v_cvt_f32_f16_sdwa v23, v23 dst_sel:DWORD dst_unused:UNUSED_PAD src0_sel:WORD_1
	v_cvt_f32_f16_e32 v24, v25
	v_cvt_f32_f16_sdwa v25, v25 dst_sel:DWORD dst_unused:UNUSED_PAD src0_sel:WORD_1
	v_fma_f32 v64, v9, v42, v64
	v_fma_f32 v65, v9, v43, v65
	v_fma_f32 v66, v9, v22, v66
	v_fma_f32 v67, v9, v23, v67
	v_fma_f32 v68, v9, v44, v68
	v_fma_f32 v69, v9, v45, v69
	v_fma_f32 v70, v9, v24, v70
	v_fma_f32 v71, v9, v25, v71
	s_and_b64 exec, s[34:35], s[34:35]
	s_cbranch_scc0 .Lhq0_s1_cp_done
	v_cvt_f32_f16_e32 v42, v26
	v_cvt_f32_f16_sdwa v43, v26 dst_sel:DWORD dst_unused:UNUSED_PAD src0_sel:WORD_1
	v_cvt_f32_f16_e32 v44, v28
	v_cvt_f32_f16_sdwa v45, v28 dst_sel:DWORD dst_unused:UNUSED_PAD src0_sel:WORD_1
	v_cvt_f32_f16_e32 v26, v27
	v_cvt_f32_f16_sdwa v27, v27 dst_sel:DWORD dst_unused:UNUSED_PAD src0_sel:WORD_1
	v_cvt_f32_f16_e32 v28, v29
	v_cvt_f32_f16_sdwa v29, v29 dst_sel:DWORD dst_unused:UNUSED_PAD src0_sel:WORD_1
	v_fma_f32 v64, v11, v42, v64
	v_fma_f32 v65, v11, v43, v65
	v_fma_f32 v66, v11, v26, v66
	v_fma_f32 v67, v11, v27, v67
	v_fma_f32 v68, v11, v44, v68
	v_fma_f32 v69, v11, v45, v69
	v_fma_f32 v70, v11, v28, v70
	v_fma_f32 v71, v11, v29, v71
	s_and_b64 exec, s[36:37], s[36:37]
	s_cbranch_scc0 .Lhq0_s1_cp_done
	v_cvt_f32_f16_e32 v42, v30
	v_cvt_f32_f16_sdwa v43, v30 dst_sel:DWORD dst_unused:UNUSED_PAD src0_sel:WORD_1
	v_cvt_f32_f16_e32 v44, v32
	v_cvt_f32_f16_sdwa v45, v32 dst_sel:DWORD dst_unused:UNUSED_PAD src0_sel:WORD_1
	v_cvt_f32_f16_e32 v30, v31
	v_cvt_f32_f16_sdwa v31, v31 dst_sel:DWORD dst_unused:UNUSED_PAD src0_sel:WORD_1
	v_cvt_f32_f16_e32 v32, v33
	v_cvt_f32_f16_sdwa v33, v33 dst_sel:DWORD dst_unused:UNUSED_PAD src0_sel:WORD_1
	v_fma_f32 v64, v13, v42, v64
	v_fma_f32 v65, v13, v43, v65
	v_fma_f32 v66, v13, v30, v66
	v_fma_f32 v67, v13, v31, v67
	v_fma_f32 v68, v13, v44, v68
	v_fma_f32 v69, v13, v45, v69
	v_fma_f32 v70, v13, v32, v70
	v_fma_f32 v71, v13, v33, v71
.Lhq0_s1_cp_done:
	s_and_b64 exec, s[42:43], s[42:43]
	s_cbranch_scc1 .Lhq0_s1_top

.Lhq0_s2_top:
	v_sub_u32_e32 v2, v5, v48
	ds_read_b64 v[6:7], v48
	ds_read_b64 v[8:9], v48 offset:8
	ds_read_b64 v[10:11], v48 offset:16
	ds_read_b64 v[12:13], v48 offset:24
	v_cmp_lt_i32_e64 s[30:31], 0, v2
	s_and_b64 s[30:31], s[30:31], exec
	s_cbranch_scc0 .Lhq0_s2_done
	v_cmp_lt_i32_e64 s[32:33], 8, v2
	v_cmp_lt_i32_e64 s[34:35], 16, v2
	v_cmp_lt_i32_e64 s[36:37], 24, v2
	v_cmp_lt_i32_e64 s[42:43], 32, v2
	v_add_u32_e32 v48, 32, v48
	v_min_i32_e32 v48, v48, v5
	s_waitcnt lgkmcnt(0)
	s_mov_b64 exec, s[30:31]
	v_lshlrev_b32_e32 v3, 7, v6
	v_and_or_b32 v3, v3, s29, v1
	global_load_dwordx4 v[18:21], v3, s[8:9]
	s_and_b64 exec, s[32:33], s[32:33]
	s_cbranch_scc0 .Lhq0_s2_ld_done
	v_lshlrev_b32_e32 v4, 7, v8
	v_and_or_b32 v4, v4, s29, v1
	global_load_dwordx4 v[22:25], v4, s[8:9]
	s_and_b64 exec, s[34:35], s[34:35]
	s_cbranch_scc0 .Lhq0_s2_ld_done
	v_lshlrev_b32_e32 v3, 7, v10
	v_and_or_b32 v3, v3, s29, v1
	global_load_dwordx4 v[26:29], v3, s[8:9]
	s_and_b64 exec, s[36:37], s[36:37]
	s_cbranch_scc0 .Lhq0_s2_ld_done
	v_lshlrev_b32_e32 v4, 7, v12
	v_and_or_b32 v4, v4, s29, v1
	global_load_dwordx4 v[30:33], v4, s[8:9]
.Lhq0_s2_ld_done:
	s_waitcnt vmcnt(0)
	s_mov_b64 exec, s[30:31]
	v_cvt_f32_f16_e32 v42, v18
	v_cvt_f32_f16_sdwa v43, v18 dst_sel:DWORD dst_unused:UNUSED_PAD src0_sel:WORD_1
	v_cvt_f32_f16_e32 v44, v20
	v_cvt_f32_f16_sdwa v45, v20 dst_sel:DWORD dst_unused:UNUSED_PAD src0_sel:WORD_1
	v_cvt_f32_f16_e32 v18, v19
	v_cvt_f32_f16_sdwa v19, v19 dst_sel:DWORD dst_unused:UNUSED_PAD src0_sel:WORD_1
	v_cvt_f32_f16_e32 v20, v21
	v_cvt_f32_f16_sdwa v21, v21 dst_sel:DWORD dst_unused:UNUSED_PAD src0_sel:WORD_1
	v_fma_f32 v72, v7, v42, v72
	v_fma_f32 v73, v7, v43, v73
	v_fma_f32 v74, v7, v18, v74
	v_fma_f32 v75, v7, v19, v75
	v_fma_f32 v76, v7, v44, v76
	v_fma_f32 v77, v7, v45, v77
	v_fma_f32 v78, v7, v20, v78
	v_fma_f32 v79, v7, v21, v79
	s_and_b64 exec, s[32:33], s[32:33]
	s_cbranch_scc0 .Lhq0_s2_cp_done
	v_cvt_f32_f16_e32 v42, v22
	v_cvt_f32_f16_sdwa v43, v22 dst_sel:DWORD dst_unused:UNUSED_PAD src0_sel:WORD_1
	v_cvt_f32_f16_e32 v44, v24
	v_cvt_f32_f16_sdwa v45, v24 dst_sel:DWORD dst_unused:UNUSED_PAD src0_sel:WORD_1
	v_cvt_f32_f16_e32 v22, v23
	v_cvt_f32_f16_sdwa v23, v23 dst_sel:DWORD dst_unused:UNUSED_PAD src0_sel:WORD_1
	v_cvt_f32_f16_e32 v24, v25
	v_cvt_f32_f16_sdwa v25, v25 dst_sel:DWORD dst_unused:UNUSED_PAD src0_sel:WORD_1
	v_fma_f32 v72, v9, v42, v72
	v_fma_f32 v73, v9, v43, v73
	v_fma_f32 v74, v9, v22, v74
	v_fma_f32 v75, v9, v23, v75
	v_fma_f32 v76, v9, v44, v76
	v_fma_f32 v77, v9, v45, v77
	v_fma_f32 v78, v9, v24, v78
	v_fma_f32 v79, v9, v25, v79
	s_and_b64 exec, s[34:35], s[34:35]
	s_cbranch_scc0 .Lhq0_s2_cp_done
	v_cvt_f32_f16_e32 v42, v26
	v_cvt_f32_f16_sdwa v43, v26 dst_sel:DWORD dst_unused:UNUSED_PAD src0_sel:WORD_1
	v_cvt_f32_f16_e32 v44, v28
	v_cvt_f32_f16_sdwa v45, v28 dst_sel:DWORD dst_unused:UNUSED_PAD src0_sel:WORD_1
	v_cvt_f32_f16_e32 v26, v27
	v_cvt_f32_f16_sdwa v27, v27 dst_sel:DWORD dst_unused:UNUSED_PAD src0_sel:WORD_1
	v_cvt_f32_f16_e32 v28, v29
	v_cvt_f32_f16_sdwa v29, v29 dst_sel:DWORD dst_unused:UNUSED_PAD src0_sel:WORD_1
	v_fma_f32 v72, v11, v42, v72
	v_fma_f32 v73, v11, v43, v73
	v_fma_f32 v74, v11, v26, v74
	v_fma_f32 v75, v11, v27, v75
	v_fma_f32 v76, v11, v44, v76
	v_fma_f32 v77, v11, v45, v77
	v_fma_f32 v78, v11, v28, v78
	v_fma_f32 v79, v11, v29, v79
	s_and_b64 exec, s[36:37], s[36:37]
	s_cbranch_scc0 .Lhq0_s2_cp_done
	v_cvt_f32_f16_e32 v42, v30
	v_cvt_f32_f16_sdwa v43, v30 dst_sel:DWORD dst_unused:UNUSED_PAD src0_sel:WORD_1
	v_cvt_f32_f16_e32 v44, v32
	v_cvt_f32_f16_sdwa v45, v32 dst_sel:DWORD dst_unused:UNUSED_PAD src0_sel:WORD_1
	v_cvt_f32_f16_e32 v30, v31
	v_cvt_f32_f16_sdwa v31, v31 dst_sel:DWORD dst_unused:UNUSED_PAD src0_sel:WORD_1
	v_cvt_f32_f16_e32 v32, v33
	v_cvt_f32_f16_sdwa v33, v33 dst_sel:DWORD dst_unused:UNUSED_PAD src0_sel:WORD_1
	v_fma_f32 v72, v13, v42, v72
	v_fma_f32 v73, v13, v43, v73
	v_fma_f32 v74, v13, v30, v74
	v_fma_f32 v75, v13, v31, v75
	v_fma_f32 v76, v13, v44, v76
	v_fma_f32 v77, v13, v45, v77
	v_fma_f32 v78, v13, v32, v78
	v_fma_f32 v79, v13, v33, v79
.Lhq0_s2_cp_done:
	s_and_b64 exec, s[42:43], s[42:43]
	s_cbranch_scc1 .Lhq0_s2_top

.Lhq0_s3_top:
	v_sub_u32_e32 v2, v5, v49
	ds_read_b64 v[6:7], v49
	ds_read_b64 v[8:9], v49 offset:8
	ds_read_b64 v[10:11], v49 offset:16
	ds_read_b64 v[12:13], v49 offset:24
	v_cmp_lt_i32_e64 s[30:31], 0, v2
	s_and_b64 s[30:31], s[30:31], exec
	s_cbranch_scc0 .Lhq0_s3_done
	v_cmp_lt_i32_e64 s[32:33], 8, v2
	v_cmp_lt_i32_e64 s[34:35], 16, v2
	v_cmp_lt_i32_e64 s[36:37], 24, v2
	v_cmp_lt_i32_e64 s[42:43], 32, v2
	v_add_u32_e32 v49, 32, v49
	v_min_i32_e32 v49, v49, v5
	s_waitcnt lgkmcnt(0)
	s_mov_b64 exec, s[30:31]
	v_lshlrev_b32_e32 v3, 7, v6
	v_and_or_b32 v3, v3, s29, v1
	global_load_dwordx4 v[18:21], v3, s[8:9]
	s_and_b64 exec, s[32:33], s[32:33]
	s_cbranch_scc0 .Lhq0_s3_ld_done
	v_lshlrev_b32_e32 v4, 7, v8
	v_and_or_b32 v4, v4, s29, v1
	global_load_dwordx4 v[22:25], v4, s[8:9]
	s_and_b64 exec, s[34:35], s[34:35]
	s_cbranch_scc0 .Lhq0_s3_ld_done
	v_lshlrev_b32_e32 v3, 7, v10
	v_and_or_b32 v3, v3, s29, v1
	global_load_dwordx4 v[26:29], v3, s[8:9]
	s_and_b64 exec, s[36:37], s[36:37]
	s_cbranch_scc0 .Lhq0_s3_ld_done
	v_lshlrev_b32_e32 v4, 7, v12
	v_and_or_b32 v4, v4, s29, v1
	global_load_dwordx4 v[30:33], v4, s[8:9]
.Lhq0_s3_ld_done:
	s_waitcnt vmcnt(0)
	s_mov_b64 exec, s[30:31]
	v_cvt_f32_f16_e32 v42, v18
	v_cvt_f32_f16_sdwa v43, v18 dst_sel:DWORD dst_unused:UNUSED_PAD src0_sel:WORD_1
	v_cvt_f32_f16_e32 v44, v20
	v_cvt_f32_f16_sdwa v45, v20 dst_sel:DWORD dst_unused:UNUSED_PAD src0_sel:WORD_1
	v_cvt_f32_f16_e32 v18, v19
	v_cvt_f32_f16_sdwa v19, v19 dst_sel:DWORD dst_unused:UNUSED_PAD src0_sel:WORD_1
	v_cvt_f32_f16_e32 v20, v21
	v_cvt_f32_f16_sdwa v21, v21 dst_sel:DWORD dst_unused:UNUSED_PAD src0_sel:WORD_1
	v_fma_f32 v80, v7, v42, v80
	v_fma_f32 v81, v7, v43, v81
	v_fma_f32 v82, v7, v18, v82
	v_fma_f32 v83, v7, v19, v83
	v_fma_f32 v84, v7, v44, v84
	v_fma_f32 v85, v7, v45, v85
	v_fma_f32 v86, v7, v20, v86
	v_fma_f32 v87, v7, v21, v87
	s_and_b64 exec, s[32:33], s[32:33]
	s_cbranch_scc0 .Lhq0_s3_cp_done
	v_cvt_f32_f16_e32 v42, v22
	v_cvt_f32_f16_sdwa v43, v22 dst_sel:DWORD dst_unused:UNUSED_PAD src0_sel:WORD_1
	v_cvt_f32_f16_e32 v44, v24
	v_cvt_f32_f16_sdwa v45, v24 dst_sel:DWORD dst_unused:UNUSED_PAD src0_sel:WORD_1
	v_cvt_f32_f16_e32 v22, v23
	v_cvt_f32_f16_sdwa v23, v23 dst_sel:DWORD dst_unused:UNUSED_PAD src0_sel:WORD_1
	v_cvt_f32_f16_e32 v24, v25
	v_cvt_f32_f16_sdwa v25, v25 dst_sel:DWORD dst_unused:UNUSED_PAD src0_sel:WORD_1
	v_fma_f32 v80, v9, v42, v80
	v_fma_f32 v81, v9, v43, v81
	v_fma_f32 v82, v9, v22, v82
	v_fma_f32 v83, v9, v23, v83
	v_fma_f32 v84, v9, v44, v84
	v_fma_f32 v85, v9, v45, v85
	v_fma_f32 v86, v9, v24, v86
	v_fma_f32 v87, v9, v25, v87
	s_and_b64 exec, s[34:35], s[34:35]
	s_cbranch_scc0 .Lhq0_s3_cp_done
	v_cvt_f32_f16_e32 v42, v26
	v_cvt_f32_f16_sdwa v43, v26 dst_sel:DWORD dst_unused:UNUSED_PAD src0_sel:WORD_1
	v_cvt_f32_f16_e32 v44, v28
	v_cvt_f32_f16_sdwa v45, v28 dst_sel:DWORD dst_unused:UNUSED_PAD src0_sel:WORD_1
	v_cvt_f32_f16_e32 v26, v27
	v_cvt_f32_f16_sdwa v27, v27 dst_sel:DWORD dst_unused:UNUSED_PAD src0_sel:WORD_1
	v_cvt_f32_f16_e32 v28, v29
	v_cvt_f32_f16_sdwa v29, v29 dst_sel:DWORD dst_unused:UNUSED_PAD src0_sel:WORD_1
	v_fma_f32 v80, v11, v42, v80
	v_fma_f32 v81, v11, v43, v81
	v_fma_f32 v82, v11, v26, v82
	v_fma_f32 v83, v11, v27, v83
	v_fma_f32 v84, v11, v44, v84
	v_fma_f32 v85, v11, v45, v85
	v_fma_f32 v86, v11, v28, v86
	v_fma_f32 v87, v11, v29, v87
	s_and_b64 exec, s[36:37], s[36:37]
	s_cbranch_scc0 .Lhq0_s3_cp_done
	v_cvt_f32_f16_e32 v42, v30
	v_cvt_f32_f16_sdwa v43, v30 dst_sel:DWORD dst_unused:UNUSED_PAD src0_sel:WORD_1
	v_cvt_f32_f16_e32 v44, v32
	v_cvt_f32_f16_sdwa v45, v32 dst_sel:DWORD dst_unused:UNUSED_PAD src0_sel:WORD_1
	v_cvt_f32_f16_e32 v30, v31
	v_cvt_f32_f16_sdwa v31, v31 dst_sel:DWORD dst_unused:UNUSED_PAD src0_sel:WORD_1
	v_cvt_f32_f16_e32 v32, v33
	v_cvt_f32_f16_sdwa v33, v33 dst_sel:DWORD dst_unused:UNUSED_PAD src0_sel:WORD_1
	v_fma_f32 v80, v13, v42, v80
	v_fma_f32 v81, v13, v43, v81
	v_fma_f32 v82, v13, v30, v82
	v_fma_f32 v83, v13, v31, v83
	v_fma_f32 v84, v13, v44, v84
	v_fma_f32 v85, v13, v45, v85
	v_fma_f32 v86, v13, v32, v86
	v_fma_f32 v87, v13, v33, v87
.Lhq0_s3_cp_done:
	s_and_b64 exec, s[42:43], s[42:43]
	s_cbranch_scc1 .Lhq0_s3_top

.Lhq0_s4_top:
	v_sub_u32_e32 v2, v5, v50
	ds_read_b64 v[6:7], v50
	ds_read_b64 v[8:9], v50 offset:8
	ds_read_b64 v[10:11], v50 offset:16
	ds_read_b64 v[12:13], v50 offset:24
	v_cmp_lt_i32_e64 s[30:31], 0, v2
	s_and_b64 s[30:31], s[30:31], exec
	s_cbranch_scc0 .Lhq0_s4_done
	v_cmp_lt_i32_e64 s[32:33], 8, v2
	v_cmp_lt_i32_e64 s[34:35], 16, v2
	v_cmp_lt_i32_e64 s[36:37], 24, v2
	v_cmp_lt_i32_e64 s[42:43], 32, v2
	v_add_u32_e32 v50, 32, v50
	v_min_i32_e32 v50, v50, v5
	s_waitcnt lgkmcnt(0)
	s_mov_b64 exec, s[30:31]
	v_lshlrev_b32_e32 v3, 7, v6
	v_and_or_b32 v3, v3, s29, v1
	global_load_dwordx4 v[18:21], v3, s[8:9]
	s_and_b64 exec, s[32:33], s[32:33]
	s_cbranch_scc0 .Lhq0_s4_ld_done
	v_lshlrev_b32_e32 v4, 7, v8
	v_and_or_b32 v4, v4, s29, v1
	global_load_dwordx4 v[22:25], v4, s[8:9]
	s_and_b64 exec, s[34:35], s[34:35]
	s_cbranch_scc0 .Lhq0_s4_ld_done
	v_lshlrev_b32_e32 v3, 7, v10
	v_and_or_b32 v3, v3, s29, v1
	global_load_dwordx4 v[26:29], v3, s[8:9]
	s_and_b64 exec, s[36:37], s[36:37]
	s_cbranch_scc0 .Lhq0_s4_ld_done
	v_lshlrev_b32_e32 v4, 7, v12
	v_and_or_b32 v4, v4, s29, v1
	global_load_dwordx4 v[30:33], v4, s[8:9]
.Lhq0_s4_ld_done:
	s_waitcnt vmcnt(0)
	s_mov_b64 exec, s[30:31]
	v_cvt_f32_f16_e32 v42, v18
	v_cvt_f32_f16_sdwa v43, v18 dst_sel:DWORD dst_unused:UNUSED_PAD src0_sel:WORD_1
	v_cvt_f32_f16_e32 v44, v20
	v_cvt_f32_f16_sdwa v45, v20 dst_sel:DWORD dst_unused:UNUSED_PAD src0_sel:WORD_1
	v_cvt_f32_f16_e32 v18, v19
	v_cvt_f32_f16_sdwa v19, v19 dst_sel:DWORD dst_unused:UNUSED_PAD src0_sel:WORD_1
	v_cvt_f32_f16_e32 v20, v21
	v_cvt_f32_f16_sdwa v21, v21 dst_sel:DWORD dst_unused:UNUSED_PAD src0_sel:WORD_1
	v_fma_f32 v88, v7, v42, v88
	v_fma_f32 v89, v7, v43, v89
	v_fma_f32 v90, v7, v18, v90
	v_fma_f32 v91, v7, v19, v91
	v_fma_f32 v92, v7, v44, v92
	v_fma_f32 v93, v7, v45, v93
	v_fma_f32 v94, v7, v20, v94
	v_fma_f32 v95, v7, v21, v95
	s_and_b64 exec, s[32:33], s[32:33]
	s_cbranch_scc0 .Lhq0_s4_cp_done
	v_cvt_f32_f16_e32 v42, v22
	v_cvt_f32_f16_sdwa v43, v22 dst_sel:DWORD dst_unused:UNUSED_PAD src0_sel:WORD_1
	v_cvt_f32_f16_e32 v44, v24
	v_cvt_f32_f16_sdwa v45, v24 dst_sel:DWORD dst_unused:UNUSED_PAD src0_sel:WORD_1
	v_cvt_f32_f16_e32 v22, v23
	v_cvt_f32_f16_sdwa v23, v23 dst_sel:DWORD dst_unused:UNUSED_PAD src0_sel:WORD_1
	v_cvt_f32_f16_e32 v24, v25
	v_cvt_f32_f16_sdwa v25, v25 dst_sel:DWORD dst_unused:UNUSED_PAD src0_sel:WORD_1
	v_fma_f32 v88, v9, v42, v88
	v_fma_f32 v89, v9, v43, v89
	v_fma_f32 v90, v9, v22, v90
	v_fma_f32 v91, v9, v23, v91
	v_fma_f32 v92, v9, v44, v92
	v_fma_f32 v93, v9, v45, v93
	v_fma_f32 v94, v9, v24, v94
	v_fma_f32 v95, v9, v25, v95
	s_and_b64 exec, s[34:35], s[34:35]
	s_cbranch_scc0 .Lhq0_s4_cp_done
	v_cvt_f32_f16_e32 v42, v26
	v_cvt_f32_f16_sdwa v43, v26 dst_sel:DWORD dst_unused:UNUSED_PAD src0_sel:WORD_1
	v_cvt_f32_f16_e32 v44, v28
	v_cvt_f32_f16_sdwa v45, v28 dst_sel:DWORD dst_unused:UNUSED_PAD src0_sel:WORD_1
	v_cvt_f32_f16_e32 v26, v27
	v_cvt_f32_f16_sdwa v27, v27 dst_sel:DWORD dst_unused:UNUSED_PAD src0_sel:WORD_1
	v_cvt_f32_f16_e32 v28, v29
	v_cvt_f32_f16_sdwa v29, v29 dst_sel:DWORD dst_unused:UNUSED_PAD src0_sel:WORD_1
	v_fma_f32 v88, v11, v42, v88
	v_fma_f32 v89, v11, v43, v89
	v_fma_f32 v90, v11, v26, v90
	v_fma_f32 v91, v11, v27, v91
	v_fma_f32 v92, v11, v44, v92
	v_fma_f32 v93, v11, v45, v93
	v_fma_f32 v94, v11, v28, v94
	v_fma_f32 v95, v11, v29, v95
	s_and_b64 exec, s[36:37], s[36:37]
	s_cbranch_scc0 .Lhq0_s4_cp_done
	v_cvt_f32_f16_e32 v42, v30
	v_cvt_f32_f16_sdwa v43, v30 dst_sel:DWORD dst_unused:UNUSED_PAD src0_sel:WORD_1
	v_cvt_f32_f16_e32 v44, v32
	v_cvt_f32_f16_sdwa v45, v32 dst_sel:DWORD dst_unused:UNUSED_PAD src0_sel:WORD_1
	v_cvt_f32_f16_e32 v30, v31
	v_cvt_f32_f16_sdwa v31, v31 dst_sel:DWORD dst_unused:UNUSED_PAD src0_sel:WORD_1
	v_cvt_f32_f16_e32 v32, v33
	v_cvt_f32_f16_sdwa v33, v33 dst_sel:DWORD dst_unused:UNUSED_PAD src0_sel:WORD_1
	v_fma_f32 v88, v13, v42, v88
	v_fma_f32 v89, v13, v43, v89
	v_fma_f32 v90, v13, v30, v90
	v_fma_f32 v91, v13, v31, v91
	v_fma_f32 v92, v13, v44, v92
	v_fma_f32 v93, v13, v45, v93
	v_fma_f32 v94, v13, v32, v94
	v_fma_f32 v95, v13, v33, v95
.Lhq0_s4_cp_done:
	s_and_b64 exec, s[42:43], s[42:43]
	s_cbranch_scc1 .Lhq0_s4_top

.Lhq0_l0_ld_done:
	s_waitcnt vmcnt(0)
	s_mov_b64 exec, s[30:31]
	v_cvt_f32_f16_e32 v42, v18
	v_cvt_f32_f16_sdwa v43, v18 dst_sel:DWORD dst_unused:UNUSED_PAD src0_sel:WORD_1
	v_cvt_f32_f16_e32 v44, v20
	v_cvt_f32_f16_sdwa v45, v20 dst_sel:DWORD dst_unused:UNUSED_PAD src0_sel:WORD_1
	v_cvt_f32_f16_e32 v18, v19
	v_cvt_f32_f16_sdwa v19, v19 dst_sel:DWORD dst_unused:UNUSED_PAD src0_sel:WORD_1
	v_cvt_f32_f16_e32 v20, v21
	v_cvt_f32_f16_sdwa v21, v21 dst_sel:DWORD dst_unused:UNUSED_PAD src0_sel:WORD_1
	v_fma_f32 v56, v7, v42, v56
	v_fma_f32 v57, v7, v43, v57
	v_fma_f32 v58, v7, v18, v58
	v_fma_f32 v59, v7, v19, v59
	v_fma_f32 v60, v7, v44, v60
	v_fma_f32 v61, v7, v45, v61
	v_fma_f32 v62, v7, v20, v62
	v_fma_f32 v63, v7, v21, v63
	s_and_b64 exec, s[32:33], s[32:33]
	s_cbranch_scc0 .Lhq0_l0_cp_done
	v_cvt_f32_f16_e32 v42, v22
	v_cvt_f32_f16_sdwa v43, v22 dst_sel:DWORD dst_unused:UNUSED_PAD src0_sel:WORD_1
	v_cvt_f32_f16_e32 v44, v24
	v_cvt_f32_f16_sdwa v45, v24 dst_sel:DWORD dst_unused:UNUSED_PAD src0_sel:WORD_1
	v_cvt_f32_f16_e32 v22, v23
	v_cvt_f32_f16_sdwa v23, v23 dst_sel:DWORD dst_unused:UNUSED_PAD src0_sel:WORD_1
	v_cvt_f32_f16_e32 v24, v25
	v_cvt_f32_f16_sdwa v25, v25 dst_sel:DWORD dst_unused:UNUSED_PAD src0_sel:WORD_1
	v_fma_f32 v56, v9, v42, v56
	v_fma_f32 v57, v9, v43, v57
	v_fma_f32 v58, v9, v22, v58
	v_fma_f32 v59, v9, v23, v59
	v_fma_f32 v60, v9, v44, v60
	v_fma_f32 v61, v9, v45, v61
	v_fma_f32 v62, v9, v24, v62
	v_fma_f32 v63, v9, v25, v63
	s_and_b64 exec, s[34:35], s[34:35]
	s_cbranch_scc0 .Lhq0_l0_cp_done
	v_cvt_f32_f16_e32 v42, v26
	v_cvt_f32_f16_sdwa v43, v26 dst_sel:DWORD dst_unused:UNUSED_PAD src0_sel:WORD_1
	v_cvt_f32_f16_e32 v44, v28
	v_cvt_f32_f16_sdwa v45, v28 dst_sel:DWORD dst_unused:UNUSED_PAD src0_sel:WORD_1
	v_cvt_f32_f16_e32 v26, v27
	v_cvt_f32_f16_sdwa v27, v27 dst_sel:DWORD dst_unused:UNUSED_PAD src0_sel:WORD_1
	v_cvt_f32_f16_e32 v28, v29
	v_cvt_f32_f16_sdwa v29, v29 dst_sel:DWORD dst_unused:UNUSED_PAD src0_sel:WORD_1
	v_fma_f32 v56, v11, v42, v56
	v_fma_f32 v57, v11, v43, v57
	v_fma_f32 v58, v11, v26, v58
	v_fma_f32 v59, v11, v27, v59
	v_fma_f32 v60, v11, v44, v60
	v_fma_f32 v61, v11, v45, v61
	v_fma_f32 v62, v11, v28, v62
	v_fma_f32 v63, v11, v29, v63
	s_and_b64 exec, s[36:37], s[36:37]
	s_cbranch_scc0 .Lhq0_l0_cp_done
	v_cvt_f32_f16_e32 v42, v30
	v_cvt_f32_f16_sdwa v43, v30 dst_sel:DWORD dst_unused:UNUSED_PAD src0_sel:WORD_1
	v_cvt_f32_f16_e32 v44, v32
	v_cvt_f32_f16_sdwa v45, v32 dst_sel:DWORD dst_unused:UNUSED_PAD src0_sel:WORD_1
	v_cvt_f32_f16_e32 v30, v31
	v_cvt_f32_f16_sdwa v31, v31 dst_sel:DWORD dst_unused:UNUSED_PAD src0_sel:WORD_1
	v_cvt_f32_f16_e32 v32, v33
	v_cvt_f32_f16_sdwa v33, v33 dst_sel:DWORD dst_unused:UNUSED_PAD src0_sel:WORD_1
	v_fma_f32 v56, v13, v42, v56
	v_fma_f32 v57, v13, v43, v57
	v_fma_f32 v58, v13, v30, v58
	v_fma_f32 v59, v13, v31, v59
	v_fma_f32 v60, v13, v44, v60
	v_fma_f32 v61, v13, v45, v61
	v_fma_f32 v62, v13, v32, v62
	v_fma_f32 v63, v13, v33, v63
.Lhq0_l0_cp_done:
	s_and_b64 exec, s[42:43], s[42:43]
	s_cbranch_scc1 .Lhq0_l0_top

.Lhq0_l1_ld_done:
	s_waitcnt vmcnt(0)
	s_mov_b64 exec, s[30:31]
	v_cvt_f32_f16_e32 v42, v18
	v_cvt_f32_f16_sdwa v43, v18 dst_sel:DWORD dst_unused:UNUSED_PAD src0_sel:WORD_1
	v_cvt_f32_f16_e32 v44, v20
	v_cvt_f32_f16_sdwa v45, v20 dst_sel:DWORD dst_unused:UNUSED_PAD src0_sel:WORD_1
	v_cvt_f32_f16_e32 v18, v19
	v_cvt_f32_f16_sdwa v19, v19 dst_sel:DWORD dst_unused:UNUSED_PAD src0_sel:WORD_1
	v_cvt_f32_f16_e32 v20, v21
	v_cvt_f32_f16_sdwa v21, v21 dst_sel:DWORD dst_unused:UNUSED_PAD src0_sel:WORD_1
	v_fma_f32 v64, v7, v42, v64
	v_fma_f32 v65, v7, v43, v65
	v_fma_f32 v66, v7, v18, v66
	v_fma_f32 v67, v7, v19, v67
	v_fma_f32 v68, v7, v44, v68
	v_fma_f32 v69, v7, v45, v69
	v_fma_f32 v70, v7, v20, v70
	v_fma_f32 v71, v7, v21, v71
	s_and_b64 exec, s[32:33], s[32:33]
	s_cbranch_scc0 .Lhq0_l1_cp_done
	v_cvt_f32_f16_e32 v42, v22
	v_cvt_f32_f16_sdwa v43, v22 dst_sel:DWORD dst_unused:UNUSED_PAD src0_sel:WORD_1
	v_cvt_f32_f16_e32 v44, v24
	v_cvt_f32_f16_sdwa v45, v24 dst_sel:DWORD dst_unused:UNUSED_PAD src0_sel:WORD_1
	v_cvt_f32_f16_e32 v22, v23
	v_cvt_f32_f16_sdwa v23, v23 dst_sel:DWORD dst_unused:UNUSED_PAD src0_sel:WORD_1
	v_cvt_f32_f16_e32 v24, v25
	v_cvt_f32_f16_sdwa v25, v25 dst_sel:DWORD dst_unused:UNUSED_PAD src0_sel:WORD_1
	v_fma_f32 v64, v9, v42, v64
	v_fma_f32 v65, v9, v43, v65
	v_fma_f32 v66, v9, v22, v66
	v_fma_f32 v67, v9, v23, v67
	v_fma_f32 v68, v9, v44, v68
	v_fma_f32 v69, v9, v45, v69
	v_fma_f32 v70, v9, v24, v70
	v_fma_f32 v71, v9, v25, v71
	s_and_b64 exec, s[34:35], s[34:35]
	s_cbranch_scc0 .Lhq0_l1_cp_done
	v_cvt_f32_f16_e32 v42, v26
	v_cvt_f32_f16_sdwa v43, v26 dst_sel:DWORD dst_unused:UNUSED_PAD src0_sel:WORD_1
	v_cvt_f32_f16_e32 v44, v28
	v_cvt_f32_f16_sdwa v45, v28 dst_sel:DWORD dst_unused:UNUSED_PAD src0_sel:WORD_1
	v_cvt_f32_f16_e32 v26, v27
	v_cvt_f32_f16_sdwa v27, v27 dst_sel:DWORD dst_unused:UNUSED_PAD src0_sel:WORD_1
	v_cvt_f32_f16_e32 v28, v29
	v_cvt_f32_f16_sdwa v29, v29 dst_sel:DWORD dst_unused:UNUSED_PAD src0_sel:WORD_1
	v_fma_f32 v64, v11, v42, v64
	v_fma_f32 v65, v11, v43, v65
	v_fma_f32 v66, v11, v26, v66
	v_fma_f32 v67, v11, v27, v67
	v_fma_f32 v68, v11, v44, v68
	v_fma_f32 v69, v11, v45, v69
	v_fma_f32 v70, v11, v28, v70
	v_fma_f32 v71, v11, v29, v71
	s_and_b64 exec, s[36:37], s[36:37]
	s_cbranch_scc0 .Lhq0_l1_cp_done
	v_cvt_f32_f16_e32 v42, v30
	v_cvt_f32_f16_sdwa v43, v30 dst_sel:DWORD dst_unused:UNUSED_PAD src0_sel:WORD_1
	v_cvt_f32_f16_e32 v44, v32
	v_cvt_f32_f16_sdwa v45, v32 dst_sel:DWORD dst_unused:UNUSED_PAD src0_sel:WORD_1
	v_cvt_f32_f16_e32 v30, v31
	v_cvt_f32_f16_sdwa v31, v31 dst_sel:DWORD dst_unused:UNUSED_PAD src0_sel:WORD_1
	v_cvt_f32_f16_e32 v32, v33
	v_cvt_f32_f16_sdwa v33, v33 dst_sel:DWORD dst_unused:UNUSED_PAD src0_sel:WORD_1
	v_fma_f32 v64, v13, v42, v64
	v_fma_f32 v65, v13, v43, v65
	v_fma_f32 v66, v13, v30, v66
	v_fma_f32 v67, v13, v31, v67
	v_fma_f32 v68, v13, v44, v68
	v_fma_f32 v69, v13, v45, v69
	v_fma_f32 v70, v13, v32, v70
	v_fma_f32 v71, v13, v33, v71
.Lhq0_l1_cp_done:
	s_and_b64 exec, s[42:43], s[42:43]
	s_cbranch_scc1 .Lhq0_l1_top

.Lhq0_l2_ld_done:
	s_waitcnt vmcnt(0)
	s_mov_b64 exec, s[30:31]
	v_cvt_f32_f16_e32 v42, v18
	v_cvt_f32_f16_sdwa v43, v18 dst_sel:DWORD dst_unused:UNUSED_PAD src0_sel:WORD_1
	v_cvt_f32_f16_e32 v44, v20
	v_cvt_f32_f16_sdwa v45, v20 dst_sel:DWORD dst_unused:UNUSED_PAD src0_sel:WORD_1
	v_cvt_f32_f16_e32 v18, v19
	v_cvt_f32_f16_sdwa v19, v19 dst_sel:DWORD dst_unused:UNUSED_PAD src0_sel:WORD_1
	v_cvt_f32_f16_e32 v20, v21
	v_cvt_f32_f16_sdwa v21, v21 dst_sel:DWORD dst_unused:UNUSED_PAD src0_sel:WORD_1
	v_fma_f32 v72, v7, v42, v72
	v_fma_f32 v73, v7, v43, v73
	v_fma_f32 v74, v7, v18, v74
	v_fma_f32 v75, v7, v19, v75
	v_fma_f32 v76, v7, v44, v76
	v_fma_f32 v77, v7, v45, v77
	v_fma_f32 v78, v7, v20, v78
	v_fma_f32 v79, v7, v21, v79
	s_and_b64 exec, s[32:33], s[32:33]
	s_cbranch_scc0 .Lhq0_l2_cp_done
	v_cvt_f32_f16_e32 v42, v22
	v_cvt_f32_f16_sdwa v43, v22 dst_sel:DWORD dst_unused:UNUSED_PAD src0_sel:WORD_1
	v_cvt_f32_f16_e32 v44, v24
	v_cvt_f32_f16_sdwa v45, v24 dst_sel:DWORD dst_unused:UNUSED_PAD src0_sel:WORD_1
	v_cvt_f32_f16_e32 v22, v23
	v_cvt_f32_f16_sdwa v23, v23 dst_sel:DWORD dst_unused:UNUSED_PAD src0_sel:WORD_1
	v_cvt_f32_f16_e32 v24, v25
	v_cvt_f32_f16_sdwa v25, v25 dst_sel:DWORD dst_unused:UNUSED_PAD src0_sel:WORD_1
	v_fma_f32 v72, v9, v42, v72
	v_fma_f32 v73, v9, v43, v73
	v_fma_f32 v74, v9, v22, v74
	v_fma_f32 v75, v9, v23, v75
	v_fma_f32 v76, v9, v44, v76
	v_fma_f32 v77, v9, v45, v77
	v_fma_f32 v78, v9, v24, v78
	v_fma_f32 v79, v9, v25, v79
	s_and_b64 exec, s[34:35], s[34:35]
	s_cbranch_scc0 .Lhq0_l2_cp_done
	v_cvt_f32_f16_e32 v42, v26
	v_cvt_f32_f16_sdwa v43, v26 dst_sel:DWORD dst_unused:UNUSED_PAD src0_sel:WORD_1
	v_cvt_f32_f16_e32 v44, v28
	v_cvt_f32_f16_sdwa v45, v28 dst_sel:DWORD dst_unused:UNUSED_PAD src0_sel:WORD_1
	v_cvt_f32_f16_e32 v26, v27
	v_cvt_f32_f16_sdwa v27, v27 dst_sel:DWORD dst_unused:UNUSED_PAD src0_sel:WORD_1
	v_cvt_f32_f16_e32 v28, v29
	v_cvt_f32_f16_sdwa v29, v29 dst_sel:DWORD dst_unused:UNUSED_PAD src0_sel:WORD_1
	v_fma_f32 v72, v11, v42, v72
	v_fma_f32 v73, v11, v43, v73
	v_fma_f32 v74, v11, v26, v74
	v_fma_f32 v75, v11, v27, v75
	v_fma_f32 v76, v11, v44, v76
	v_fma_f32 v77, v11, v45, v77
	v_fma_f32 v78, v11, v28, v78
	v_fma_f32 v79, v11, v29, v79
	s_and_b64 exec, s[36:37], s[36:37]
	s_cbranch_scc0 .Lhq0_l2_cp_done
	v_cvt_f32_f16_e32 v42, v30
	v_cvt_f32_f16_sdwa v43, v30 dst_sel:DWORD dst_unused:UNUSED_PAD src0_sel:WORD_1
	v_cvt_f32_f16_e32 v44, v32
	v_cvt_f32_f16_sdwa v45, v32 dst_sel:DWORD dst_unused:UNUSED_PAD src0_sel:WORD_1
	v_cvt_f32_f16_e32 v30, v31
	v_cvt_f32_f16_sdwa v31, v31 dst_sel:DWORD dst_unused:UNUSED_PAD src0_sel:WORD_1
	v_cvt_f32_f16_e32 v32, v33
	v_cvt_f32_f16_sdwa v33, v33 dst_sel:DWORD dst_unused:UNUSED_PAD src0_sel:WORD_1
	v_fma_f32 v72, v13, v42, v72
	v_fma_f32 v73, v13, v43, v73
	v_fma_f32 v74, v13, v30, v74
	v_fma_f32 v75, v13, v31, v75
	v_fma_f32 v76, v13, v44, v76
	v_fma_f32 v77, v13, v45, v77
	v_fma_f32 v78, v13, v32, v78
	v_fma_f32 v79, v13, v33, v79
.Lhq0_l2_cp_done:
	s_and_b64 exec, s[42:43], s[42:43]
	s_cbranch_scc1 .Lhq0_l2_top

.Lhq0_l3_ld_done:
	s_waitcnt vmcnt(0)
	s_mov_b64 exec, s[30:31]
	v_cvt_f32_f16_e32 v42, v18
	v_cvt_f32_f16_sdwa v43, v18 dst_sel:DWORD dst_unused:UNUSED_PAD src0_sel:WORD_1
	v_cvt_f32_f16_e32 v44, v20
	v_cvt_f32_f16_sdwa v45, v20 dst_sel:DWORD dst_unused:UNUSED_PAD src0_sel:WORD_1
	v_cvt_f32_f16_e32 v18, v19
	v_cvt_f32_f16_sdwa v19, v19 dst_sel:DWORD dst_unused:UNUSED_PAD src0_sel:WORD_1
	v_cvt_f32_f16_e32 v20, v21
	v_cvt_f32_f16_sdwa v21, v21 dst_sel:DWORD dst_unused:UNUSED_PAD src0_sel:WORD_1
	v_fma_f32 v80, v7, v42, v80
	v_fma_f32 v81, v7, v43, v81
	v_fma_f32 v82, v7, v18, v82
	v_fma_f32 v83, v7, v19, v83
	v_fma_f32 v84, v7, v44, v84
	v_fma_f32 v85, v7, v45, v85
	v_fma_f32 v86, v7, v20, v86
	v_fma_f32 v87, v7, v21, v87
	s_and_b64 exec, s[32:33], s[32:33]
	s_cbranch_scc0 .Lhq0_l3_cp_done
	v_cvt_f32_f16_e32 v42, v22
	v_cvt_f32_f16_sdwa v43, v22 dst_sel:DWORD dst_unused:UNUSED_PAD src0_sel:WORD_1
	v_cvt_f32_f16_e32 v44, v24
	v_cvt_f32_f16_sdwa v45, v24 dst_sel:DWORD dst_unused:UNUSED_PAD src0_sel:WORD_1
	v_cvt_f32_f16_e32 v22, v23
	v_cvt_f32_f16_sdwa v23, v23 dst_sel:DWORD dst_unused:UNUSED_PAD src0_sel:WORD_1
	v_cvt_f32_f16_e32 v24, v25
	v_cvt_f32_f16_sdwa v25, v25 dst_sel:DWORD dst_unused:UNUSED_PAD src0_sel:WORD_1
	v_fma_f32 v80, v9, v42, v80
	v_fma_f32 v81, v9, v43, v81
	v_fma_f32 v82, v9, v22, v82
	v_fma_f32 v83, v9, v23, v83
	v_fma_f32 v84, v9, v44, v84
	v_fma_f32 v85, v9, v45, v85
	v_fma_f32 v86, v9, v24, v86
	v_fma_f32 v87, v9, v25, v87
	s_and_b64 exec, s[34:35], s[34:35]
	s_cbranch_scc0 .Lhq0_l3_cp_done
	v_cvt_f32_f16_e32 v42, v26
	v_cvt_f32_f16_sdwa v43, v26 dst_sel:DWORD dst_unused:UNUSED_PAD src0_sel:WORD_1
	v_cvt_f32_f16_e32 v44, v28
	v_cvt_f32_f16_sdwa v45, v28 dst_sel:DWORD dst_unused:UNUSED_PAD src0_sel:WORD_1
	v_cvt_f32_f16_e32 v26, v27
	v_cvt_f32_f16_sdwa v27, v27 dst_sel:DWORD dst_unused:UNUSED_PAD src0_sel:WORD_1
	v_cvt_f32_f16_e32 v28, v29
	v_cvt_f32_f16_sdwa v29, v29 dst_sel:DWORD dst_unused:UNUSED_PAD src0_sel:WORD_1
	v_fma_f32 v80, v11, v42, v80
	v_fma_f32 v81, v11, v43, v81
	v_fma_f32 v82, v11, v26, v82
	v_fma_f32 v83, v11, v27, v83
	v_fma_f32 v84, v11, v44, v84
	v_fma_f32 v85, v11, v45, v85
	v_fma_f32 v86, v11, v28, v86
	v_fma_f32 v87, v11, v29, v87
	s_and_b64 exec, s[36:37], s[36:37]
	s_cbranch_scc0 .Lhq0_l3_cp_done
	v_cvt_f32_f16_e32 v42, v30
	v_cvt_f32_f16_sdwa v43, v30 dst_sel:DWORD dst_unused:UNUSED_PAD src0_sel:WORD_1
	v_cvt_f32_f16_e32 v44, v32
	v_cvt_f32_f16_sdwa v45, v32 dst_sel:DWORD dst_unused:UNUSED_PAD src0_sel:WORD_1
	v_cvt_f32_f16_e32 v30, v31
	v_cvt_f32_f16_sdwa v31, v31 dst_sel:DWORD dst_unused:UNUSED_PAD src0_sel:WORD_1
	v_cvt_f32_f16_e32 v32, v33
	v_cvt_f32_f16_sdwa v33, v33 dst_sel:DWORD dst_unused:UNUSED_PAD src0_sel:WORD_1
	v_fma_f32 v80, v13, v42, v80
	v_fma_f32 v81, v13, v43, v81
	v_fma_f32 v82, v13, v30, v82
	v_fma_f32 v83, v13, v31, v83
	v_fma_f32 v84, v13, v44, v84
	v_fma_f32 v85, v13, v45, v85
	v_fma_f32 v86, v13, v32, v86
	v_fma_f32 v87, v13, v33, v87
.Lhq0_l3_cp_done:
	s_and_b64 exec, s[42:43], s[42:43]
	s_cbranch_scc1 .Lhq0_l3_top

.Lhq0_l4_ld_done:
	s_waitcnt vmcnt(0)
	s_mov_b64 exec, s[30:31]
	v_cvt_f32_f16_e32 v42, v18
	v_cvt_f32_f16_sdwa v43, v18 dst_sel:DWORD dst_unused:UNUSED_PAD src0_sel:WORD_1
	v_cvt_f32_f16_e32 v44, v20
	v_cvt_f32_f16_sdwa v45, v20 dst_sel:DWORD dst_unused:UNUSED_PAD src0_sel:WORD_1
	v_cvt_f32_f16_e32 v18, v19
	v_cvt_f32_f16_sdwa v19, v19 dst_sel:DWORD dst_unused:UNUSED_PAD src0_sel:WORD_1
	v_cvt_f32_f16_e32 v20, v21
	v_cvt_f32_f16_sdwa v21, v21 dst_sel:DWORD dst_unused:UNUSED_PAD src0_sel:WORD_1
	v_fma_f32 v88, v7, v42, v88
	v_fma_f32 v89, v7, v43, v89
	v_fma_f32 v90, v7, v18, v90
	v_fma_f32 v91, v7, v19, v91
	v_fma_f32 v92, v7, v44, v92
	v_fma_f32 v93, v7, v45, v93
	v_fma_f32 v94, v7, v20, v94
	v_fma_f32 v95, v7, v21, v95
	s_and_b64 exec, s[32:33], s[32:33]
	s_cbranch_scc0 .Lhq0_l4_cp_done
	v_cvt_f32_f16_e32 v42, v22
	v_cvt_f32_f16_sdwa v43, v22 dst_sel:DWORD dst_unused:UNUSED_PAD src0_sel:WORD_1
	v_cvt_f32_f16_e32 v44, v24
	v_cvt_f32_f16_sdwa v45, v24 dst_sel:DWORD dst_unused:UNUSED_PAD src0_sel:WORD_1
	v_cvt_f32_f16_e32 v22, v23
	v_cvt_f32_f16_sdwa v23, v23 dst_sel:DWORD dst_unused:UNUSED_PAD src0_sel:WORD_1
	v_cvt_f32_f16_e32 v24, v25
	v_cvt_f32_f16_sdwa v25, v25 dst_sel:DWORD dst_unused:UNUSED_PAD src0_sel:WORD_1
	v_fma_f32 v88, v9, v42, v88
	v_fma_f32 v89, v9, v43, v89
	v_fma_f32 v90, v9, v22, v90
	v_fma_f32 v91, v9, v23, v91
	v_fma_f32 v92, v9, v44, v92
	v_fma_f32 v93, v9, v45, v93
	v_fma_f32 v94, v9, v24, v94
	v_fma_f32 v95, v9, v25, v95
	s_and_b64 exec, s[34:35], s[34:35]
	s_cbranch_scc0 .Lhq0_l4_cp_done
	v_cvt_f32_f16_e32 v42, v26
	v_cvt_f32_f16_sdwa v43, v26 dst_sel:DWORD dst_unused:UNUSED_PAD src0_sel:WORD_1
	v_cvt_f32_f16_e32 v44, v28
	v_cvt_f32_f16_sdwa v45, v28 dst_sel:DWORD dst_unused:UNUSED_PAD src0_sel:WORD_1
	v_cvt_f32_f16_e32 v26, v27
	v_cvt_f32_f16_sdwa v27, v27 dst_sel:DWORD dst_unused:UNUSED_PAD src0_sel:WORD_1
	v_cvt_f32_f16_e32 v28, v29
	v_cvt_f32_f16_sdwa v29, v29 dst_sel:DWORD dst_unused:UNUSED_PAD src0_sel:WORD_1
	v_fma_f32 v88, v11, v42, v88
	v_fma_f32 v89, v11, v43, v89
	v_fma_f32 v90, v11, v26, v90
	v_fma_f32 v91, v11, v27, v91
	v_fma_f32 v92, v11, v44, v92
	v_fma_f32 v93, v11, v45, v93
	v_fma_f32 v94, v11, v28, v94
	v_fma_f32 v95, v11, v29, v95
	s_and_b64 exec, s[36:37], s[36:37]
	s_cbranch_scc0 .Lhq0_l4_cp_done
	v_cvt_f32_f16_e32 v42, v30
	v_cvt_f32_f16_sdwa v43, v30 dst_sel:DWORD dst_unused:UNUSED_PAD src0_sel:WORD_1
	v_cvt_f32_f16_e32 v44, v32
	v_cvt_f32_f16_sdwa v45, v32 dst_sel:DWORD dst_unused:UNUSED_PAD src0_sel:WORD_1
	v_cvt_f32_f16_e32 v30, v31
	v_cvt_f32_f16_sdwa v31, v31 dst_sel:DWORD dst_unused:UNUSED_PAD src0_sel:WORD_1
	v_cvt_f32_f16_e32 v32, v33
	v_cvt_f32_f16_sdwa v33, v33 dst_sel:DWORD dst_unused:UNUSED_PAD src0_sel:WORD_1
	v_fma_f32 v88, v13, v42, v88
	v_fma_f32 v89, v13, v43, v89
	v_fma_f32 v90, v13, v30, v90
	v_fma_f32 v91, v13, v31, v91
	v_fma_f32 v92, v13, v44, v92
	v_fma_f32 v93, v13, v45, v93
	v_fma_f32 v94, v13, v32, v94
	v_fma_f32 v95, v13, v33, v95
.Lhq0_l4_cp_done:
	s_and_b64 exec, s[42:43], s[42:43]
	s_cbranch_scc1 .Lhq0_l4_top

.Lhq1_s0_ld_done:
	s_waitcnt vmcnt(0)
	s_mov_b64 exec, s[30:31]
	v_cvt_f32_f16_e32 v42, v18
	v_cvt_f32_f16_sdwa v43, v18 dst_sel:DWORD dst_unused:UNUSED_PAD src0_sel:WORD_1
	v_cvt_f32_f16_e32 v44, v20
	v_cvt_f32_f16_sdwa v45, v20 dst_sel:DWORD dst_unused:UNUSED_PAD src0_sel:WORD_1
	v_cvt_f32_f16_e32 v18, v19
	v_cvt_f32_f16_sdwa v19, v19 dst_sel:DWORD dst_unused:UNUSED_PAD src0_sel:WORD_1
	v_cvt_f32_f16_e32 v20, v21
	v_cvt_f32_f16_sdwa v21, v21 dst_sel:DWORD dst_unused:UNUSED_PAD src0_sel:WORD_1
	v_fma_f32 v56, v7, v42, v56
	v_fma_f32 v57, v7, v43, v57
	v_fma_f32 v58, v7, v18, v58
	v_fma_f32 v59, v7, v19, v59
	v_fma_f32 v60, v7, v44, v60
	v_fma_f32 v61, v7, v45, v61
	v_fma_f32 v62, v7, v20, v62
	v_fma_f32 v63, v7, v21, v63
	s_and_b64 exec, s[32:33], s[32:33]
	s_cbranch_scc0 .Lhq1_s0_cp_done
	v_cvt_f32_f16_e32 v42, v22
	v_cvt_f32_f16_sdwa v43, v22 dst_sel:DWORD dst_unused:UNUSED_PAD src0_sel:WORD_1
	v_cvt_f32_f16_e32 v44, v24
	v_cvt_f32_f16_sdwa v45, v24 dst_sel:DWORD dst_unused:UNUSED_PAD src0_sel:WORD_1
	v_cvt_f32_f16_e32 v22, v23
	v_cvt_f32_f16_sdwa v23, v23 dst_sel:DWORD dst_unused:UNUSED_PAD src0_sel:WORD_1
	v_cvt_f32_f16_e32 v24, v25
	v_cvt_f32_f16_sdwa v25, v25 dst_sel:DWORD dst_unused:UNUSED_PAD src0_sel:WORD_1
	v_fma_f32 v56, v9, v42, v56
	v_fma_f32 v57, v9, v43, v57
	v_fma_f32 v58, v9, v22, v58
	v_fma_f32 v59, v9, v23, v59
	v_fma_f32 v60, v9, v44, v60
	v_fma_f32 v61, v9, v45, v61
	v_fma_f32 v62, v9, v24, v62
	v_fma_f32 v63, v9, v25, v63
	s_and_b64 exec, s[34:35], s[34:35]
	s_cbranch_scc0 .Lhq1_s0_cp_done
	v_cvt_f32_f16_e32 v42, v26
	v_cvt_f32_f16_sdwa v43, v26 dst_sel:DWORD dst_unused:UNUSED_PAD src0_sel:WORD_1
	v_cvt_f32_f16_e32 v44, v28
	v_cvt_f32_f16_sdwa v45, v28 dst_sel:DWORD dst_unused:UNUSED_PAD src0_sel:WORD_1
	v_cvt_f32_f16_e32 v26, v27
	v_cvt_f32_f16_sdwa v27, v27 dst_sel:DWORD dst_unused:UNUSED_PAD src0_sel:WORD_1
	v_cvt_f32_f16_e32 v28, v29
	v_cvt_f32_f16_sdwa v29, v29 dst_sel:DWORD dst_unused:UNUSED_PAD src0_sel:WORD_1
	v_fma_f32 v56, v11, v42, v56
	v_fma_f32 v57, v11, v43, v57
	v_fma_f32 v58, v11, v26, v58
	v_fma_f32 v59, v11, v27, v59
	v_fma_f32 v60, v11, v44, v60
	v_fma_f32 v61, v11, v45, v61
	v_fma_f32 v62, v11, v28, v62
	v_fma_f32 v63, v11, v29, v63
	s_and_b64 exec, s[36:37], s[36:37]
	s_cbranch_scc0 .Lhq1_s0_cp_done
	v_cvt_f32_f16_e32 v42, v30
	v_cvt_f32_f16_sdwa v43, v30 dst_sel:DWORD dst_unused:UNUSED_PAD src0_sel:WORD_1
	v_cvt_f32_f16_e32 v44, v32
	v_cvt_f32_f16_sdwa v45, v32 dst_sel:DWORD dst_unused:UNUSED_PAD src0_sel:WORD_1
	v_cvt_f32_f16_e32 v30, v31
	v_cvt_f32_f16_sdwa v31, v31 dst_sel:DWORD dst_unused:UNUSED_PAD src0_sel:WORD_1
	v_cvt_f32_f16_e32 v32, v33
	v_cvt_f32_f16_sdwa v33, v33 dst_sel:DWORD dst_unused:UNUSED_PAD src0_sel:WORD_1
	v_fma_f32 v56, v13, v42, v56
	v_fma_f32 v57, v13, v43, v57
	v_fma_f32 v58, v13, v30, v58
	v_fma_f32 v59, v13, v31, v59
	v_fma_f32 v60, v13, v44, v60
	v_fma_f32 v61, v13, v45, v61
	v_fma_f32 v62, v13, v32, v62
	v_fma_f32 v63, v13, v33, v63
.Lhq1_s0_cp_done:
	s_and_b64 exec, s[42:43], s[42:43]
	s_cbranch_scc1 .Lhq1_s0_top

.Lhq1_s1_ld_done:
	s_waitcnt vmcnt(0)
	s_mov_b64 exec, s[30:31]
	v_cvt_f32_f16_e32 v42, v18
	v_cvt_f32_f16_sdwa v43, v18 dst_sel:DWORD dst_unused:UNUSED_PAD src0_sel:WORD_1
	v_cvt_f32_f16_e32 v44, v20
	v_cvt_f32_f16_sdwa v45, v20 dst_sel:DWORD dst_unused:UNUSED_PAD src0_sel:WORD_1
	v_cvt_f32_f16_e32 v18, v19
	v_cvt_f32_f16_sdwa v19, v19 dst_sel:DWORD dst_unused:UNUSED_PAD src0_sel:WORD_1
	v_cvt_f32_f16_e32 v20, v21
	v_cvt_f32_f16_sdwa v21, v21 dst_sel:DWORD dst_unused:UNUSED_PAD src0_sel:WORD_1
	v_fma_f32 v64, v7, v42, v64
	v_fma_f32 v65, v7, v43, v65
	v_fma_f32 v66, v7, v18, v66
	v_fma_f32 v67, v7, v19, v67
	v_fma_f32 v68, v7, v44, v68
	v_fma_f32 v69, v7, v45, v69
	v_fma_f32 v70, v7, v20, v70
	v_fma_f32 v71, v7, v21, v71
	s_and_b64 exec, s[32:33], s[32:33]
	s_cbranch_scc0 .Lhq1_s1_cp_done
	v_cvt_f32_f16_e32 v42, v22
	v_cvt_f32_f16_sdwa v43, v22 dst_sel:DWORD dst_unused:UNUSED_PAD src0_sel:WORD_1
	v_cvt_f32_f16_e32 v44, v24
	v_cvt_f32_f16_sdwa v45, v24 dst_sel:DWORD dst_unused:UNUSED_PAD src0_sel:WORD_1
	v_cvt_f32_f16_e32 v22, v23
	v_cvt_f32_f16_sdwa v23, v23 dst_sel:DWORD dst_unused:UNUSED_PAD src0_sel:WORD_1
	v_cvt_f32_f16_e32 v24, v25
	v_cvt_f32_f16_sdwa v25, v25 dst_sel:DWORD dst_unused:UNUSED_PAD src0_sel:WORD_1
	v_fma_f32 v64, v9, v42, v64
	v_fma_f32 v65, v9, v43, v65
	v_fma_f32 v66, v9, v22, v66
	v_fma_f32 v67, v9, v23, v67
	v_fma_f32 v68, v9, v44, v68
	v_fma_f32 v69, v9, v45, v69
	v_fma_f32 v70, v9, v24, v70
	v_fma_f32 v71, v9, v25, v71
	s_and_b64 exec, s[34:35], s[34:35]
	s_cbranch_scc0 .Lhq1_s1_cp_done
	v_cvt_f32_f16_e32 v42, v26
	v_cvt_f32_f16_sdwa v43, v26 dst_sel:DWORD dst_unused:UNUSED_PAD src0_sel:WORD_1
	v_cvt_f32_f16_e32 v44, v28
	v_cvt_f32_f16_sdwa v45, v28 dst_sel:DWORD dst_unused:UNUSED_PAD src0_sel:WORD_1
	v_cvt_f32_f16_e32 v26, v27
	v_cvt_f32_f16_sdwa v27, v27 dst_sel:DWORD dst_unused:UNUSED_PAD src0_sel:WORD_1
	v_cvt_f32_f16_e32 v28, v29
	v_cvt_f32_f16_sdwa v29, v29 dst_sel:DWORD dst_unused:UNUSED_PAD src0_sel:WORD_1
	v_fma_f32 v64, v11, v42, v64
	v_fma_f32 v65, v11, v43, v65
	v_fma_f32 v66, v11, v26, v66
	v_fma_f32 v67, v11, v27, v67
	v_fma_f32 v68, v11, v44, v68
	v_fma_f32 v69, v11, v45, v69
	v_fma_f32 v70, v11, v28, v70
	v_fma_f32 v71, v11, v29, v71
	s_and_b64 exec, s[36:37], s[36:37]
	s_cbranch_scc0 .Lhq1_s1_cp_done
	v_cvt_f32_f16_e32 v42, v30
	v_cvt_f32_f16_sdwa v43, v30 dst_sel:DWORD dst_unused:UNUSED_PAD src0_sel:WORD_1
	v_cvt_f32_f16_e32 v44, v32
	v_cvt_f32_f16_sdwa v45, v32 dst_sel:DWORD dst_unused:UNUSED_PAD src0_sel:WORD_1
	v_cvt_f32_f16_e32 v30, v31
	v_cvt_f32_f16_sdwa v31, v31 dst_sel:DWORD dst_unused:UNUSED_PAD src0_sel:WORD_1
	v_cvt_f32_f16_e32 v32, v33
	v_cvt_f32_f16_sdwa v33, v33 dst_sel:DWORD dst_unused:UNUSED_PAD src0_sel:WORD_1
	v_fma_f32 v64, v13, v42, v64
	v_fma_f32 v65, v13, v43, v65
	v_fma_f32 v66, v13, v30, v66
	v_fma_f32 v67, v13, v31, v67
	v_fma_f32 v68, v13, v44, v68
	v_fma_f32 v69, v13, v45, v69
	v_fma_f32 v70, v13, v32, v70
	v_fma_f32 v71, v13, v33, v71
.Lhq1_s1_cp_done:
	s_and_b64 exec, s[42:43], s[42:43]
	s_cbranch_scc1 .Lhq1_s1_top

.Lhq1_s2_ld_done:
	s_waitcnt vmcnt(0)
	s_mov_b64 exec, s[30:31]
	v_cvt_f32_f16_e32 v42, v18
	v_cvt_f32_f16_sdwa v43, v18 dst_sel:DWORD dst_unused:UNUSED_PAD src0_sel:WORD_1
	v_cvt_f32_f16_e32 v44, v20
	v_cvt_f32_f16_sdwa v45, v20 dst_sel:DWORD dst_unused:UNUSED_PAD src0_sel:WORD_1
	v_cvt_f32_f16_e32 v18, v19
	v_cvt_f32_f16_sdwa v19, v19 dst_sel:DWORD dst_unused:UNUSED_PAD src0_sel:WORD_1
	v_cvt_f32_f16_e32 v20, v21
	v_cvt_f32_f16_sdwa v21, v21 dst_sel:DWORD dst_unused:UNUSED_PAD src0_sel:WORD_1
	v_fma_f32 v72, v7, v42, v72
	v_fma_f32 v73, v7, v43, v73
	v_fma_f32 v74, v7, v18, v74
	v_fma_f32 v75, v7, v19, v75
	v_fma_f32 v76, v7, v44, v76
	v_fma_f32 v77, v7, v45, v77
	v_fma_f32 v78, v7, v20, v78
	v_fma_f32 v79, v7, v21, v79
	s_and_b64 exec, s[32:33], s[32:33]
	s_cbranch_scc0 .Lhq1_s2_cp_done
	v_cvt_f32_f16_e32 v42, v22
	v_cvt_f32_f16_sdwa v43, v22 dst_sel:DWORD dst_unused:UNUSED_PAD src0_sel:WORD_1
	v_cvt_f32_f16_e32 v44, v24
	v_cvt_f32_f16_sdwa v45, v24 dst_sel:DWORD dst_unused:UNUSED_PAD src0_sel:WORD_1
	v_cvt_f32_f16_e32 v22, v23
	v_cvt_f32_f16_sdwa v23, v23 dst_sel:DWORD dst_unused:UNUSED_PAD src0_sel:WORD_1
	v_cvt_f32_f16_e32 v24, v25
	v_cvt_f32_f16_sdwa v25, v25 dst_sel:DWORD dst_unused:UNUSED_PAD src0_sel:WORD_1
	v_fma_f32 v72, v9, v42, v72
	v_fma_f32 v73, v9, v43, v73
	v_fma_f32 v74, v9, v22, v74
	v_fma_f32 v75, v9, v23, v75
	v_fma_f32 v76, v9, v44, v76
	v_fma_f32 v77, v9, v45, v77
	v_fma_f32 v78, v9, v24, v78
	v_fma_f32 v79, v9, v25, v79
	s_and_b64 exec, s[34:35], s[34:35]
	s_cbranch_scc0 .Lhq1_s2_cp_done
	v_cvt_f32_f16_e32 v42, v26
	v_cvt_f32_f16_sdwa v43, v26 dst_sel:DWORD dst_unused:UNUSED_PAD src0_sel:WORD_1
	v_cvt_f32_f16_e32 v44, v28
	v_cvt_f32_f16_sdwa v45, v28 dst_sel:DWORD dst_unused:UNUSED_PAD src0_sel:WORD_1
	v_cvt_f32_f16_e32 v26, v27
	v_cvt_f32_f16_sdwa v27, v27 dst_sel:DWORD dst_unused:UNUSED_PAD src0_sel:WORD_1
	v_cvt_f32_f16_e32 v28, v29
	v_cvt_f32_f16_sdwa v29, v29 dst_sel:DWORD dst_unused:UNUSED_PAD src0_sel:WORD_1
	v_fma_f32 v72, v11, v42, v72
	v_fma_f32 v73, v11, v43, v73
	v_fma_f32 v74, v11, v26, v74
	v_fma_f32 v75, v11, v27, v75
	v_fma_f32 v76, v11, v44, v76
	v_fma_f32 v77, v11, v45, v77
	v_fma_f32 v78, v11, v28, v78
	v_fma_f32 v79, v11, v29, v79
	s_and_b64 exec, s[36:37], s[36:37]
	s_cbranch_scc0 .Lhq1_s2_cp_done
	v_cvt_f32_f16_e32 v42, v30
	v_cvt_f32_f16_sdwa v43, v30 dst_sel:DWORD dst_unused:UNUSED_PAD src0_sel:WORD_1
	v_cvt_f32_f16_e32 v44, v32
	v_cvt_f32_f16_sdwa v45, v32 dst_sel:DWORD dst_unused:UNUSED_PAD src0_sel:WORD_1
	v_cvt_f32_f16_e32 v30, v31
	v_cvt_f32_f16_sdwa v31, v31 dst_sel:DWORD dst_unused:UNUSED_PAD src0_sel:WORD_1
	v_cvt_f32_f16_e32 v32, v33
	v_cvt_f32_f16_sdwa v33, v33 dst_sel:DWORD dst_unused:UNUSED_PAD src0_sel:WORD_1
	v_fma_f32 v72, v13, v42, v72
	v_fma_f32 v73, v13, v43, v73
	v_fma_f32 v74, v13, v30, v74
	v_fma_f32 v75, v13, v31, v75
	v_fma_f32 v76, v13, v44, v76
	v_fma_f32 v77, v13, v45, v77
	v_fma_f32 v78, v13, v32, v78
	v_fma_f32 v79, v13, v33, v79
.Lhq1_s2_cp_done:
	s_and_b64 exec, s[42:43], s[42:43]
	s_cbranch_scc1 .Lhq1_s2_top

.Lhq1_s3_ld_done:
	s_waitcnt vmcnt(0)
	s_mov_b64 exec, s[30:31]
	v_cvt_f32_f16_e32 v42, v18
	v_cvt_f32_f16_sdwa v43, v18 dst_sel:DWORD dst_unused:UNUSED_PAD src0_sel:WORD_1
	v_cvt_f32_f16_e32 v44, v20
	v_cvt_f32_f16_sdwa v45, v20 dst_sel:DWORD dst_unused:UNUSED_PAD src0_sel:WORD_1
	v_cvt_f32_f16_e32 v18, v19
	v_cvt_f32_f16_sdwa v19, v19 dst_sel:DWORD dst_unused:UNUSED_PAD src0_sel:WORD_1
	v_cvt_f32_f16_e32 v20, v21
	v_cvt_f32_f16_sdwa v21, v21 dst_sel:DWORD dst_unused:UNUSED_PAD src0_sel:WORD_1
	v_fma_f32 v80, v7, v42, v80
	v_fma_f32 v81, v7, v43, v81
	v_fma_f32 v82, v7, v18, v82
	v_fma_f32 v83, v7, v19, v83
	v_fma_f32 v84, v7, v44, v84
	v_fma_f32 v85, v7, v45, v85
	v_fma_f32 v86, v7, v20, v86
	v_fma_f32 v87, v7, v21, v87
	s_and_b64 exec, s[32:33], s[32:33]
	s_cbranch_scc0 .Lhq1_s3_cp_done
	v_cvt_f32_f16_e32 v42, v22
	v_cvt_f32_f16_sdwa v43, v22 dst_sel:DWORD dst_unused:UNUSED_PAD src0_sel:WORD_1
	v_cvt_f32_f16_e32 v44, v24
	v_cvt_f32_f16_sdwa v45, v24 dst_sel:DWORD dst_unused:UNUSED_PAD src0_sel:WORD_1
	v_cvt_f32_f16_e32 v22, v23
	v_cvt_f32_f16_sdwa v23, v23 dst_sel:DWORD dst_unused:UNUSED_PAD src0_sel:WORD_1
	v_cvt_f32_f16_e32 v24, v25
	v_cvt_f32_f16_sdwa v25, v25 dst_sel:DWORD dst_unused:UNUSED_PAD src0_sel:WORD_1
	v_fma_f32 v80, v9, v42, v80
	v_fma_f32 v81, v9, v43, v81
	v_fma_f32 v82, v9, v22, v82
	v_fma_f32 v83, v9, v23, v83
	v_fma_f32 v84, v9, v44, v84
	v_fma_f32 v85, v9, v45, v85
	v_fma_f32 v86, v9, v24, v86
	v_fma_f32 v87, v9, v25, v87
	s_and_b64 exec, s[34:35], s[34:35]
	s_cbranch_scc0 .Lhq1_s3_cp_done
	v_cvt_f32_f16_e32 v42, v26
	v_cvt_f32_f16_sdwa v43, v26 dst_sel:DWORD dst_unused:UNUSED_PAD src0_sel:WORD_1
	v_cvt_f32_f16_e32 v44, v28
	v_cvt_f32_f16_sdwa v45, v28 dst_sel:DWORD dst_unused:UNUSED_PAD src0_sel:WORD_1
	v_cvt_f32_f16_e32 v26, v27
	v_cvt_f32_f16_sdwa v27, v27 dst_sel:DWORD dst_unused:UNUSED_PAD src0_sel:WORD_1
	v_cvt_f32_f16_e32 v28, v29
	v_cvt_f32_f16_sdwa v29, v29 dst_sel:DWORD dst_unused:UNUSED_PAD src0_sel:WORD_1
	v_fma_f32 v80, v11, v42, v80
	v_fma_f32 v81, v11, v43, v81
	v_fma_f32 v82, v11, v26, v82
	v_fma_f32 v83, v11, v27, v83
	v_fma_f32 v84, v11, v44, v84
	v_fma_f32 v85, v11, v45, v85
	v_fma_f32 v86, v11, v28, v86
	v_fma_f32 v87, v11, v29, v87
	s_and_b64 exec, s[36:37], s[36:37]
	s_cbranch_scc0 .Lhq1_s3_cp_done
	v_cvt_f32_f16_e32 v42, v30
	v_cvt_f32_f16_sdwa v43, v30 dst_sel:DWORD dst_unused:UNUSED_PAD src0_sel:WORD_1
	v_cvt_f32_f16_e32 v44, v32
	v_cvt_f32_f16_sdwa v45, v32 dst_sel:DWORD dst_unused:UNUSED_PAD src0_sel:WORD_1
	v_cvt_f32_f16_e32 v30, v31
	v_cvt_f32_f16_sdwa v31, v31 dst_sel:DWORD dst_unused:UNUSED_PAD src0_sel:WORD_1
	v_cvt_f32_f16_e32 v32, v33
	v_cvt_f32_f16_sdwa v33, v33 dst_sel:DWORD dst_unused:UNUSED_PAD src0_sel:WORD_1
	v_fma_f32 v80, v13, v42, v80
	v_fma_f32 v81, v13, v43, v81
	v_fma_f32 v82, v13, v30, v82
	v_fma_f32 v83, v13, v31, v83
	v_fma_f32 v84, v13, v44, v84
	v_fma_f32 v85, v13, v45, v85
	v_fma_f32 v86, v13, v32, v86
	v_fma_f32 v87, v13, v33, v87
.Lhq1_s3_cp_done:
	s_and_b64 exec, s[42:43], s[42:43]
	s_cbranch_scc1 .Lhq1_s3_top

.Lhq1_s4_ld_done:
	s_waitcnt vmcnt(0)
	s_mov_b64 exec, s[30:31]
	v_cvt_f32_f16_e32 v42, v18
	v_cvt_f32_f16_sdwa v43, v18 dst_sel:DWORD dst_unused:UNUSED_PAD src0_sel:WORD_1
	v_cvt_f32_f16_e32 v44, v20
	v_cvt_f32_f16_sdwa v45, v20 dst_sel:DWORD dst_unused:UNUSED_PAD src0_sel:WORD_1
	v_cvt_f32_f16_e32 v18, v19
	v_cvt_f32_f16_sdwa v19, v19 dst_sel:DWORD dst_unused:UNUSED_PAD src0_sel:WORD_1
	v_cvt_f32_f16_e32 v20, v21
	v_cvt_f32_f16_sdwa v21, v21 dst_sel:DWORD dst_unused:UNUSED_PAD src0_sel:WORD_1
	v_fma_f32 v88, v7, v42, v88
	v_fma_f32 v89, v7, v43, v89
	v_fma_f32 v90, v7, v18, v90
	v_fma_f32 v91, v7, v19, v91
	v_fma_f32 v92, v7, v44, v92
	v_fma_f32 v93, v7, v45, v93
	v_fma_f32 v94, v7, v20, v94
	v_fma_f32 v95, v7, v21, v95
	s_and_b64 exec, s[32:33], s[32:33]
	s_cbranch_scc0 .Lhq1_s4_cp_done
	v_cvt_f32_f16_e32 v42, v22
	v_cvt_f32_f16_sdwa v43, v22 dst_sel:DWORD dst_unused:UNUSED_PAD src0_sel:WORD_1
	v_cvt_f32_f16_e32 v44, v24
	v_cvt_f32_f16_sdwa v45, v24 dst_sel:DWORD dst_unused:UNUSED_PAD src0_sel:WORD_1
	v_cvt_f32_f16_e32 v22, v23
	v_cvt_f32_f16_sdwa v23, v23 dst_sel:DWORD dst_unused:UNUSED_PAD src0_sel:WORD_1
	v_cvt_f32_f16_e32 v24, v25
	v_cvt_f32_f16_sdwa v25, v25 dst_sel:DWORD dst_unused:UNUSED_PAD src0_sel:WORD_1
	v_fma_f32 v88, v9, v42, v88
	v_fma_f32 v89, v9, v43, v89
	v_fma_f32 v90, v9, v22, v90
	v_fma_f32 v91, v9, v23, v91
	v_fma_f32 v92, v9, v44, v92
	v_fma_f32 v93, v9, v45, v93
	v_fma_f32 v94, v9, v24, v94
	v_fma_f32 v95, v9, v25, v95
	s_and_b64 exec, s[34:35], s[34:35]
	s_cbranch_scc0 .Lhq1_s4_cp_done
	v_cvt_f32_f16_e32 v42, v26
	v_cvt_f32_f16_sdwa v43, v26 dst_sel:DWORD dst_unused:UNUSED_PAD src0_sel:WORD_1
	v_cvt_f32_f16_e32 v44, v28
	v_cvt_f32_f16_sdwa v45, v28 dst_sel:DWORD dst_unused:UNUSED_PAD src0_sel:WORD_1
	v_cvt_f32_f16_e32 v26, v27
	v_cvt_f32_f16_sdwa v27, v27 dst_sel:DWORD dst_unused:UNUSED_PAD src0_sel:WORD_1
	v_cvt_f32_f16_e32 v28, v29
	v_cvt_f32_f16_sdwa v29, v29 dst_sel:DWORD dst_unused:UNUSED_PAD src0_sel:WORD_1
	v_fma_f32 v88, v11, v42, v88
	v_fma_f32 v89, v11, v43, v89
	v_fma_f32 v90, v11, v26, v90
	v_fma_f32 v91, v11, v27, v91
	v_fma_f32 v92, v11, v44, v92
	v_fma_f32 v93, v11, v45, v93
	v_fma_f32 v94, v11, v28, v94
	v_fma_f32 v95, v11, v29, v95
	s_and_b64 exec, s[36:37], s[36:37]
	s_cbranch_scc0 .Lhq1_s4_cp_done
	v_cvt_f32_f16_e32 v42, v30
	v_cvt_f32_f16_sdwa v43, v30 dst_sel:DWORD dst_unused:UNUSED_PAD src0_sel:WORD_1
	v_cvt_f32_f16_e32 v44, v32
	v_cvt_f32_f16_sdwa v45, v32 dst_sel:DWORD dst_unused:UNUSED_PAD src0_sel:WORD_1
	v_cvt_f32_f16_e32 v30, v31
	v_cvt_f32_f16_sdwa v31, v31 dst_sel:DWORD dst_unused:UNUSED_PAD src0_sel:WORD_1
	v_cvt_f32_f16_e32 v32, v33
	v_cvt_f32_f16_sdwa v33, v33 dst_sel:DWORD dst_unused:UNUSED_PAD src0_sel:WORD_1
	v_fma_f32 v88, v13, v42, v88
	v_fma_f32 v89, v13, v43, v89
	v_fma_f32 v90, v13, v30, v90
	v_fma_f32 v91, v13, v31, v91
	v_fma_f32 v92, v13, v44, v92
	v_fma_f32 v93, v13, v45, v93
	v_fma_f32 v94, v13, v32, v94
	v_fma_f32 v95, v13, v33, v95
.Lhq1_s4_cp_done:
	s_and_b64 exec, s[42:43], s[42:43]
	s_cbranch_scc1 .Lhq1_s4_top

.Lhq1_l0_ld_done:
	s_waitcnt vmcnt(0)
	s_mov_b64 exec, s[30:31]
	v_cvt_f32_f16_e32 v42, v18
	v_cvt_f32_f16_sdwa v43, v18 dst_sel:DWORD dst_unused:UNUSED_PAD src0_sel:WORD_1
	v_cvt_f32_f16_e32 v44, v20
	v_cvt_f32_f16_sdwa v45, v20 dst_sel:DWORD dst_unused:UNUSED_PAD src0_sel:WORD_1
	v_cvt_f32_f16_e32 v18, v19
	v_cvt_f32_f16_sdwa v19, v19 dst_sel:DWORD dst_unused:UNUSED_PAD src0_sel:WORD_1
	v_cvt_f32_f16_e32 v20, v21
	v_cvt_f32_f16_sdwa v21, v21 dst_sel:DWORD dst_unused:UNUSED_PAD src0_sel:WORD_1
	v_fma_f32 v56, v7, v42, v56
	v_fma_f32 v57, v7, v43, v57
	v_fma_f32 v58, v7, v18, v58
	v_fma_f32 v59, v7, v19, v59
	v_fma_f32 v60, v7, v44, v60
	v_fma_f32 v61, v7, v45, v61
	v_fma_f32 v62, v7, v20, v62
	v_fma_f32 v63, v7, v21, v63
	s_and_b64 exec, s[32:33], s[32:33]
	s_cbranch_scc0 .Lhq1_l0_cp_done
	v_cvt_f32_f16_e32 v42, v22
	v_cvt_f32_f16_sdwa v43, v22 dst_sel:DWORD dst_unused:UNUSED_PAD src0_sel:WORD_1
	v_cvt_f32_f16_e32 v44, v24
	v_cvt_f32_f16_sdwa v45, v24 dst_sel:DWORD dst_unused:UNUSED_PAD src0_sel:WORD_1
	v_cvt_f32_f16_e32 v22, v23
	v_cvt_f32_f16_sdwa v23, v23 dst_sel:DWORD dst_unused:UNUSED_PAD src0_sel:WORD_1
	v_cvt_f32_f16_e32 v24, v25
	v_cvt_f32_f16_sdwa v25, v25 dst_sel:DWORD dst_unused:UNUSED_PAD src0_sel:WORD_1
	v_fma_f32 v56, v9, v42, v56
	v_fma_f32 v57, v9, v43, v57
	v_fma_f32 v58, v9, v22, v58
	v_fma_f32 v59, v9, v23, v59
	v_fma_f32 v60, v9, v44, v60
	v_fma_f32 v61, v9, v45, v61
	v_fma_f32 v62, v9, v24, v62
	v_fma_f32 v63, v9, v25, v63
	s_and_b64 exec, s[34:35], s[34:35]
	s_cbranch_scc0 .Lhq1_l0_cp_done
	v_cvt_f32_f16_e32 v42, v26
	v_cvt_f32_f16_sdwa v43, v26 dst_sel:DWORD dst_unused:UNUSED_PAD src0_sel:WORD_1
	v_cvt_f32_f16_e32 v44, v28
	v_cvt_f32_f16_sdwa v45, v28 dst_sel:DWORD dst_unused:UNUSED_PAD src0_sel:WORD_1
	v_cvt_f32_f16_e32 v26, v27
	v_cvt_f32_f16_sdwa v27, v27 dst_sel:DWORD dst_unused:UNUSED_PAD src0_sel:WORD_1
	v_cvt_f32_f16_e32 v28, v29
	v_cvt_f32_f16_sdwa v29, v29 dst_sel:DWORD dst_unused:UNUSED_PAD src0_sel:WORD_1
	v_fma_f32 v56, v11, v42, v56
	v_fma_f32 v57, v11, v43, v57
	v_fma_f32 v58, v11, v26, v58
	v_fma_f32 v59, v11, v27, v59
	v_fma_f32 v60, v11, v44, v60
	v_fma_f32 v61, v11, v45, v61
	v_fma_f32 v62, v11, v28, v62
	v_fma_f32 v63, v11, v29, v63
	s_and_b64 exec, s[36:37], s[36:37]
	s_cbranch_scc0 .Lhq1_l0_cp_done
	v_cvt_f32_f16_e32 v42, v30
	v_cvt_f32_f16_sdwa v43, v30 dst_sel:DWORD dst_unused:UNUSED_PAD src0_sel:WORD_1
	v_cvt_f32_f16_e32 v44, v32
	v_cvt_f32_f16_sdwa v45, v32 dst_sel:DWORD dst_unused:UNUSED_PAD src0_sel:WORD_1
	v_cvt_f32_f16_e32 v30, v31
	v_cvt_f32_f16_sdwa v31, v31 dst_sel:DWORD dst_unused:UNUSED_PAD src0_sel:WORD_1
	v_cvt_f32_f16_e32 v32, v33
	v_cvt_f32_f16_sdwa v33, v33 dst_sel:DWORD dst_unused:UNUSED_PAD src0_sel:WORD_1
	v_fma_f32 v56, v13, v42, v56
	v_fma_f32 v57, v13, v43, v57
	v_fma_f32 v58, v13, v30, v58
	v_fma_f32 v59, v13, v31, v59
	v_fma_f32 v60, v13, v44, v60
	v_fma_f32 v61, v13, v45, v61
	v_fma_f32 v62, v13, v32, v62
	v_fma_f32 v63, v13, v33, v63
.Lhq1_l0_cp_done:
	s_and_b64 exec, s[42:43], s[42:43]
	s_cbranch_scc1 .Lhq1_l0_top

.Lhq1_l1_ld_done:
	s_waitcnt vmcnt(0)
	s_mov_b64 exec, s[30:31]
	v_cvt_f32_f16_e32 v42, v18
	v_cvt_f32_f16_sdwa v43, v18 dst_sel:DWORD dst_unused:UNUSED_PAD src0_sel:WORD_1
	v_cvt_f32_f16_e32 v44, v20
	v_cvt_f32_f16_sdwa v45, v20 dst_sel:DWORD dst_unused:UNUSED_PAD src0_sel:WORD_1
	v_cvt_f32_f16_e32 v18, v19
	v_cvt_f32_f16_sdwa v19, v19 dst_sel:DWORD dst_unused:UNUSED_PAD src0_sel:WORD_1
	v_cvt_f32_f16_e32 v20, v21
	v_cvt_f32_f16_sdwa v21, v21 dst_sel:DWORD dst_unused:UNUSED_PAD src0_sel:WORD_1
	v_fma_f32 v64, v7, v42, v64
	v_fma_f32 v65, v7, v43, v65
	v_fma_f32 v66, v7, v18, v66
	v_fma_f32 v67, v7, v19, v67
	v_fma_f32 v68, v7, v44, v68
	v_fma_f32 v69, v7, v45, v69
	v_fma_f32 v70, v7, v20, v70
	v_fma_f32 v71, v7, v21, v71
	s_and_b64 exec, s[32:33], s[32:33]
	s_cbranch_scc0 .Lhq1_l1_cp_done
	v_cvt_f32_f16_e32 v42, v22
	v_cvt_f32_f16_sdwa v43, v22 dst_sel:DWORD dst_unused:UNUSED_PAD src0_sel:WORD_1
	v_cvt_f32_f16_e32 v44, v24
	v_cvt_f32_f16_sdwa v45, v24 dst_sel:DWORD dst_unused:UNUSED_PAD src0_sel:WORD_1
	v_cvt_f32_f16_e32 v22, v23
	v_cvt_f32_f16_sdwa v23, v23 dst_sel:DWORD dst_unused:UNUSED_PAD src0_sel:WORD_1
	v_cvt_f32_f16_e32 v24, v25
	v_cvt_f32_f16_sdwa v25, v25 dst_sel:DWORD dst_unused:UNUSED_PAD src0_sel:WORD_1
	v_fma_f32 v64, v9, v42, v64
	v_fma_f32 v65, v9, v43, v65
	v_fma_f32 v66, v9, v22, v66
	v_fma_f32 v67, v9, v23, v67
	v_fma_f32 v68, v9, v44, v68
	v_fma_f32 v69, v9, v45, v69
	v_fma_f32 v70, v9, v24, v70
	v_fma_f32 v71, v9, v25, v71
	s_and_b64 exec, s[34:35], s[34:35]
	s_cbranch_scc0 .Lhq1_l1_cp_done
	v_cvt_f32_f16_e32 v42, v26
	v_cvt_f32_f16_sdwa v43, v26 dst_sel:DWORD dst_unused:UNUSED_PAD src0_sel:WORD_1
	v_cvt_f32_f16_e32 v44, v28
	v_cvt_f32_f16_sdwa v45, v28 dst_sel:DWORD dst_unused:UNUSED_PAD src0_sel:WORD_1
	v_cvt_f32_f16_e32 v26, v27
	v_cvt_f32_f16_sdwa v27, v27 dst_sel:DWORD dst_unused:UNUSED_PAD src0_sel:WORD_1
	v_cvt_f32_f16_e32 v28, v29
	v_cvt_f32_f16_sdwa v29, v29 dst_sel:DWORD dst_unused:UNUSED_PAD src0_sel:WORD_1
	v_fma_f32 v64, v11, v42, v64
	v_fma_f32 v65, v11, v43, v65
	v_fma_f32 v66, v11, v26, v66
	v_fma_f32 v67, v11, v27, v67
	v_fma_f32 v68, v11, v44, v68
	v_fma_f32 v69, v11, v45, v69
	v_fma_f32 v70, v11, v28, v70
	v_fma_f32 v71, v11, v29, v71
	s_and_b64 exec, s[36:37], s[36:37]
	s_cbranch_scc0 .Lhq1_l1_cp_done
	v_cvt_f32_f16_e32 v42, v30
	v_cvt_f32_f16_sdwa v43, v30 dst_sel:DWORD dst_unused:UNUSED_PAD src0_sel:WORD_1
	v_cvt_f32_f16_e32 v44, v32
	v_cvt_f32_f16_sdwa v45, v32 dst_sel:DWORD dst_unused:UNUSED_PAD src0_sel:WORD_1
	v_cvt_f32_f16_e32 v30, v31
	v_cvt_f32_f16_sdwa v31, v31 dst_sel:DWORD dst_unused:UNUSED_PAD src0_sel:WORD_1
	v_cvt_f32_f16_e32 v32, v33
	v_cvt_f32_f16_sdwa v33, v33 dst_sel:DWORD dst_unused:UNUSED_PAD src0_sel:WORD_1
	v_fma_f32 v64, v13, v42, v64
	v_fma_f32 v65, v13, v43, v65
	v_fma_f32 v66, v13, v30, v66
	v_fma_f32 v67, v13, v31, v67
	v_fma_f32 v68, v13, v44, v68
	v_fma_f32 v69, v13, v45, v69
	v_fma_f32 v70, v13, v32, v70
	v_fma_f32 v71, v13, v33, v71
.Lhq1_l1_cp_done:
	s_and_b64 exec, s[42:43], s[42:43]
	s_cbranch_scc1 .Lhq1_l1_top

.Lhq1_l2_ld_done:
	s_waitcnt vmcnt(0)
	s_mov_b64 exec, s[30:31]
	v_cvt_f32_f16_e32 v42, v18
	v_cvt_f32_f16_sdwa v43, v18 dst_sel:DWORD dst_unused:UNUSED_PAD src0_sel:WORD_1
	v_cvt_f32_f16_e32 v44, v20
	v_cvt_f32_f16_sdwa v45, v20 dst_sel:DWORD dst_unused:UNUSED_PAD src0_sel:WORD_1
	v_cvt_f32_f16_e32 v18, v19
	v_cvt_f32_f16_sdwa v19, v19 dst_sel:DWORD dst_unused:UNUSED_PAD src0_sel:WORD_1
	v_cvt_f32_f16_e32 v20, v21
	v_cvt_f32_f16_sdwa v21, v21 dst_sel:DWORD dst_unused:UNUSED_PAD src0_sel:WORD_1
	v_fma_f32 v72, v7, v42, v72
	v_fma_f32 v73, v7, v43, v73
	v_fma_f32 v74, v7, v18, v74
	v_fma_f32 v75, v7, v19, v75
	v_fma_f32 v76, v7, v44, v76
	v_fma_f32 v77, v7, v45, v77
	v_fma_f32 v78, v7, v20, v78
	v_fma_f32 v79, v7, v21, v79
	s_and_b64 exec, s[32:33], s[32:33]
	s_cbranch_scc0 .Lhq1_l2_cp_done
	v_cvt_f32_f16_e32 v42, v22
	v_cvt_f32_f16_sdwa v43, v22 dst_sel:DWORD dst_unused:UNUSED_PAD src0_sel:WORD_1
	v_cvt_f32_f16_e32 v44, v24
	v_cvt_f32_f16_sdwa v45, v24 dst_sel:DWORD dst_unused:UNUSED_PAD src0_sel:WORD_1
	v_cvt_f32_f16_e32 v22, v23
	v_cvt_f32_f16_sdwa v23, v23 dst_sel:DWORD dst_unused:UNUSED_PAD src0_sel:WORD_1
	v_cvt_f32_f16_e32 v24, v25
	v_cvt_f32_f16_sdwa v25, v25 dst_sel:DWORD dst_unused:UNUSED_PAD src0_sel:WORD_1
	v_fma_f32 v72, v9, v42, v72
	v_fma_f32 v73, v9, v43, v73
	v_fma_f32 v74, v9, v22, v74
	v_fma_f32 v75, v9, v23, v75
	v_fma_f32 v76, v9, v44, v76
	v_fma_f32 v77, v9, v45, v77
	v_fma_f32 v78, v9, v24, v78
	v_fma_f32 v79, v9, v25, v79
	s_and_b64 exec, s[34:35], s[34:35]
	s_cbranch_scc0 .Lhq1_l2_cp_done
	v_cvt_f32_f16_e32 v42, v26
	v_cvt_f32_f16_sdwa v43, v26 dst_sel:DWORD dst_unused:UNUSED_PAD src0_sel:WORD_1
	v_cvt_f32_f16_e32 v44, v28
	v_cvt_f32_f16_sdwa v45, v28 dst_sel:DWORD dst_unused:UNUSED_PAD src0_sel:WORD_1
	v_cvt_f32_f16_e32 v26, v27
	v_cvt_f32_f16_sdwa v27, v27 dst_sel:DWORD dst_unused:UNUSED_PAD src0_sel:WORD_1
	v_cvt_f32_f16_e32 v28, v29
	v_cvt_f32_f16_sdwa v29, v29 dst_sel:DWORD dst_unused:UNUSED_PAD src0_sel:WORD_1
	v_fma_f32 v72, v11, v42, v72
	v_fma_f32 v73, v11, v43, v73
	v_fma_f32 v74, v11, v26, v74
	v_fma_f32 v75, v11, v27, v75
	v_fma_f32 v76, v11, v44, v76
	v_fma_f32 v77, v11, v45, v77
	v_fma_f32 v78, v11, v28, v78
	v_fma_f32 v79, v11, v29, v79
	s_and_b64 exec, s[36:37], s[36:37]
	s_cbranch_scc0 .Lhq1_l2_cp_done
	v_cvt_f32_f16_e32 v42, v30
	v_cvt_f32_f16_sdwa v43, v30 dst_sel:DWORD dst_unused:UNUSED_PAD src0_sel:WORD_1
	v_cvt_f32_f16_e32 v44, v32
	v_cvt_f32_f16_sdwa v45, v32 dst_sel:DWORD dst_unused:UNUSED_PAD src0_sel:WORD_1
	v_cvt_f32_f16_e32 v30, v31
	v_cvt_f32_f16_sdwa v31, v31 dst_sel:DWORD dst_unused:UNUSED_PAD src0_sel:WORD_1
	v_cvt_f32_f16_e32 v32, v33
	v_cvt_f32_f16_sdwa v33, v33 dst_sel:DWORD dst_unused:UNUSED_PAD src0_sel:WORD_1
	v_fma_f32 v72, v13, v42, v72
	v_fma_f32 v73, v13, v43, v73
	v_fma_f32 v74, v13, v30, v74
	v_fma_f32 v75, v13, v31, v75
	v_fma_f32 v76, v13, v44, v76
	v_fma_f32 v77, v13, v45, v77
	v_fma_f32 v78, v13, v32, v78
	v_fma_f32 v79, v13, v33, v79
.Lhq1_l2_cp_done:
	s_and_b64 exec, s[42:43], s[42:43]
	s_cbranch_scc1 .Lhq1_l2_top

.Lhq1_l3_ld_done:
	s_waitcnt vmcnt(0)
	s_mov_b64 exec, s[30:31]
	v_cvt_f32_f16_e32 v42, v18
	v_cvt_f32_f16_sdwa v43, v18 dst_sel:DWORD dst_unused:UNUSED_PAD src0_sel:WORD_1
	v_cvt_f32_f16_e32 v44, v20
	v_cvt_f32_f16_sdwa v45, v20 dst_sel:DWORD dst_unused:UNUSED_PAD src0_sel:WORD_1
	v_cvt_f32_f16_e32 v18, v19
	v_cvt_f32_f16_sdwa v19, v19 dst_sel:DWORD dst_unused:UNUSED_PAD src0_sel:WORD_1
	v_cvt_f32_f16_e32 v20, v21
	v_cvt_f32_f16_sdwa v21, v21 dst_sel:DWORD dst_unused:UNUSED_PAD src0_sel:WORD_1
	v_fma_f32 v80, v7, v42, v80
	v_fma_f32 v81, v7, v43, v81
	v_fma_f32 v82, v7, v18, v82
	v_fma_f32 v83, v7, v19, v83
	v_fma_f32 v84, v7, v44, v84
	v_fma_f32 v85, v7, v45, v85
	v_fma_f32 v86, v7, v20, v86
	v_fma_f32 v87, v7, v21, v87
	s_and_b64 exec, s[32:33], s[32:33]
	s_cbranch_scc0 .Lhq1_l3_cp_done
	v_cvt_f32_f16_e32 v42, v22
	v_cvt_f32_f16_sdwa v43, v22 dst_sel:DWORD dst_unused:UNUSED_PAD src0_sel:WORD_1
	v_cvt_f32_f16_e32 v44, v24
	v_cvt_f32_f16_sdwa v45, v24 dst_sel:DWORD dst_unused:UNUSED_PAD src0_sel:WORD_1
	v_cvt_f32_f16_e32 v22, v23
	v_cvt_f32_f16_sdwa v23, v23 dst_sel:DWORD dst_unused:UNUSED_PAD src0_sel:WORD_1
	v_cvt_f32_f16_e32 v24, v25
	v_cvt_f32_f16_sdwa v25, v25 dst_sel:DWORD dst_unused:UNUSED_PAD src0_sel:WORD_1
	v_fma_f32 v80, v9, v42, v80
	v_fma_f32 v81, v9, v43, v81
	v_fma_f32 v82, v9, v22, v82
	v_fma_f32 v83, v9, v23, v83
	v_fma_f32 v84, v9, v44, v84
	v_fma_f32 v85, v9, v45, v85
	v_fma_f32 v86, v9, v24, v86
	v_fma_f32 v87, v9, v25, v87
	s_and_b64 exec, s[34:35], s[34:35]
	s_cbranch_scc0 .Lhq1_l3_cp_done
	v_cvt_f32_f16_e32 v42, v26
	v_cvt_f32_f16_sdwa v43, v26 dst_sel:DWORD dst_unused:UNUSED_PAD src0_sel:WORD_1
	v_cvt_f32_f16_e32 v44, v28
	v_cvt_f32_f16_sdwa v45, v28 dst_sel:DWORD dst_unused:UNUSED_PAD src0_sel:WORD_1
	v_cvt_f32_f16_e32 v26, v27
	v_cvt_f32_f16_sdwa v27, v27 dst_sel:DWORD dst_unused:UNUSED_PAD src0_sel:WORD_1
	v_cvt_f32_f16_e32 v28, v29
	v_cvt_f32_f16_sdwa v29, v29 dst_sel:DWORD dst_unused:UNUSED_PAD src0_sel:WORD_1
	v_fma_f32 v80, v11, v42, v80
	v_fma_f32 v81, v11, v43, v81
	v_fma_f32 v82, v11, v26, v82
	v_fma_f32 v83, v11, v27, v83
	v_fma_f32 v84, v11, v44, v84
	v_fma_f32 v85, v11, v45, v85
	v_fma_f32 v86, v11, v28, v86
	v_fma_f32 v87, v11, v29, v87
	s_and_b64 exec, s[36:37], s[36:37]
	s_cbranch_scc0 .Lhq1_l3_cp_done
	v_cvt_f32_f16_e32 v42, v30
	v_cvt_f32_f16_sdwa v43, v30 dst_sel:DWORD dst_unused:UNUSED_PAD src0_sel:WORD_1
	v_cvt_f32_f16_e32 v44, v32
	v_cvt_f32_f16_sdwa v45, v32 dst_sel:DWORD dst_unused:UNUSED_PAD src0_sel:WORD_1
	v_cvt_f32_f16_e32 v30, v31
	v_cvt_f32_f16_sdwa v31, v31 dst_sel:DWORD dst_unused:UNUSED_PAD src0_sel:WORD_1
	v_cvt_f32_f16_e32 v32, v33
	v_cvt_f32_f16_sdwa v33, v33 dst_sel:DWORD dst_unused:UNUSED_PAD src0_sel:WORD_1
	v_fma_f32 v80, v13, v42, v80
	v_fma_f32 v81, v13, v43, v81
	v_fma_f32 v82, v13, v30, v82
	v_fma_f32 v83, v13, v31, v83
	v_fma_f32 v84, v13, v44, v84
	v_fma_f32 v85, v13, v45, v85
	v_fma_f32 v86, v13, v32, v86
	v_fma_f32 v87, v13, v33, v87
.Lhq1_l3_cp_done:
	s_and_b64 exec, s[42:43], s[42:43]
	s_cbranch_scc1 .Lhq1_l3_top

.Lhq1_l4_ld_done:
	s_waitcnt vmcnt(0)
	s_mov_b64 exec, s[30:31]
	v_cvt_f32_f16_e32 v42, v18
	v_cvt_f32_f16_sdwa v43, v18 dst_sel:DWORD dst_unused:UNUSED_PAD src0_sel:WORD_1
	v_cvt_f32_f16_e32 v44, v20
	v_cvt_f32_f16_sdwa v45, v20 dst_sel:DWORD dst_unused:UNUSED_PAD src0_sel:WORD_1
	v_cvt_f32_f16_e32 v18, v19
	v_cvt_f32_f16_sdwa v19, v19 dst_sel:DWORD dst_unused:UNUSED_PAD src0_sel:WORD_1
	v_cvt_f32_f16_e32 v20, v21
	v_cvt_f32_f16_sdwa v21, v21 dst_sel:DWORD dst_unused:UNUSED_PAD src0_sel:WORD_1
	v_fma_f32 v88, v7, v42, v88
	v_fma_f32 v89, v7, v43, v89
	v_fma_f32 v90, v7, v18, v90
	v_fma_f32 v91, v7, v19, v91
	v_fma_f32 v92, v7, v44, v92
	v_fma_f32 v93, v7, v45, v93
	v_fma_f32 v94, v7, v20, v94
	v_fma_f32 v95, v7, v21, v95
	s_and_b64 exec, s[32:33], s[32:33]
	s_cbranch_scc0 .Lhq1_l4_cp_done
	v_cvt_f32_f16_e32 v42, v22
	v_cvt_f32_f16_sdwa v43, v22 dst_sel:DWORD dst_unused:UNUSED_PAD src0_sel:WORD_1
	v_cvt_f32_f16_e32 v44, v24
	v_cvt_f32_f16_sdwa v45, v24 dst_sel:DWORD dst_unused:UNUSED_PAD src0_sel:WORD_1
	v_cvt_f32_f16_e32 v22, v23
	v_cvt_f32_f16_sdwa v23, v23 dst_sel:DWORD dst_unused:UNUSED_PAD src0_sel:WORD_1
	v_cvt_f32_f16_e32 v24, v25
	v_cvt_f32_f16_sdwa v25, v25 dst_sel:DWORD dst_unused:UNUSED_PAD src0_sel:WORD_1
	v_fma_f32 v88, v9, v42, v88
	v_fma_f32 v89, v9, v43, v89
	v_fma_f32 v90, v9, v22, v90
	v_fma_f32 v91, v9, v23, v91
	v_fma_f32 v92, v9, v44, v92
	v_fma_f32 v93, v9, v45, v93
	v_fma_f32 v94, v9, v24, v94
	v_fma_f32 v95, v9, v25, v95
	s_and_b64 exec, s[34:35], s[34:35]
	s_cbranch_scc0 .Lhq1_l4_cp_done
	v_cvt_f32_f16_e32 v42, v26
	v_cvt_f32_f16_sdwa v43, v26 dst_sel:DWORD dst_unused:UNUSED_PAD src0_sel:WORD_1
	v_cvt_f32_f16_e32 v44, v28
	v_cvt_f32_f16_sdwa v45, v28 dst_sel:DWORD dst_unused:UNUSED_PAD src0_sel:WORD_1
	v_cvt_f32_f16_e32 v26, v27
	v_cvt_f32_f16_sdwa v27, v27 dst_sel:DWORD dst_unused:UNUSED_PAD src0_sel:WORD_1
	v_cvt_f32_f16_e32 v28, v29
	v_cvt_f32_f16_sdwa v29, v29 dst_sel:DWORD dst_unused:UNUSED_PAD src0_sel:WORD_1
	v_fma_f32 v88, v11, v42, v88
	v_fma_f32 v89, v11, v43, v89
	v_fma_f32 v90, v11, v26, v90
	v_fma_f32 v91, v11, v27, v91
	v_fma_f32 v92, v11, v44, v92
	v_fma_f32 v93, v11, v45, v93
	v_fma_f32 v94, v11, v28, v94
	v_fma_f32 v95, v11, v29, v95
	s_and_b64 exec, s[36:37], s[36:37]
	s_cbranch_scc0 .Lhq1_l4_cp_done
	v_cvt_f32_f16_e32 v42, v30
	v_cvt_f32_f16_sdwa v43, v30 dst_sel:DWORD dst_unused:UNUSED_PAD src0_sel:WORD_1
	v_cvt_f32_f16_e32 v44, v32
	v_cvt_f32_f16_sdwa v45, v32 dst_sel:DWORD dst_unused:UNUSED_PAD src0_sel:WORD_1
	v_cvt_f32_f16_e32 v30, v31
	v_cvt_f32_f16_sdwa v31, v31 dst_sel:DWORD dst_unused:UNUSED_PAD src0_sel:WORD_1
	v_cvt_f32_f16_e32 v32, v33
	v_cvt_f32_f16_sdwa v33, v33 dst_sel:DWORD dst_unused:UNUSED_PAD src0_sel:WORD_1
	v_fma_f32 v88, v13, v42, v88
	v_fma_f32 v89, v13, v43, v89
	v_fma_f32 v90, v13, v30, v90
	v_fma_f32 v91, v13, v31, v91
	v_fma_f32 v92, v13, v44, v92
	v_fma_f32 v93, v13, v45, v93
	v_fma_f32 v94, v13, v32, v94
	v_fma_f32 v95, v13, v33, v95
.Lhq1_l4_cp_done:
	s_and_b64 exec, s[42:43], s[42:43]
	s_cbranch_scc1 .Lhq1_l4_top
